# lever 9 loop-edge: in the 8 GEMM K-loops the counter/address bumps and exit test moved in front of the loop-back barrier
# baseline (speedup 1.0000x reference)
; #define PG8_STAGE(bufoff, gbase, voff) do { _Pragma("unroll") for (int _i = 0; _i < 2; ++_i) \
;         __builtin_amdgcn_global_load_lds((const unsigned*)((const char*)(gbase) + (voff)[_i]), (PG8_LAS unsigned*)(lds + (bufoff) + ldsw + _i * 8192), 16, 0, 0); } while (0)
; #define PG8_STAGE_A(bufoff, gbase, h, nx) do { if constexpr (Sched::GATHER) { const unsigned vv_[2] = {(nx) ? vAn[h][0] : vA[h][0], (nx) ? vAn[h][1] : vA[h][1]}; PG8_STAGE(bufoff, gbase, vv_); } \
;         else { PG8_STAGE(bufoff, (gbase) + (h) * hstep, voffA); } } while (0)
; #define PG8_LDA(dst, b, h) do { _Pragma("unroll") for (int m = 0; m < 4; ++m) _Pragma("unroll") for (int k = 0; k < 2; ++k) dst[m][k] = *(const PG8_LAS bf16x8*)(lds + PG8_SA(b, h) + aoff + m * 2048 + k * 1024); } while (0)
; #define PG8_LDB(dst, b, h) do { _Pragma("unroll") for (int n = 0; n < 2; ++n) _Pragma("unroll") for (int k = 0; k < 2; ++k) dst[n][k] = *(const PG8_LAS bf16x8*)(lds + PG8_SB(b, h) + boff + n * 2048 + k * 1024); } while (0)
; #define PG8_WAIT_V(n) asm volatile("s_waitcnt vmcnt(" #n ")" ::: "memory")
; #define PG8_WAIT_L(n) asm volatile("s_waitcnt lgkmcnt(" #n ")" ::: "memory")
; #define PG8_BAR __builtin_amdgcn_s_barrier()
; #define PG8_SCHED __builtin_amdgcn_sched_barrier(0)
;     ...
;         for (int t = 0; t < nt; t += 2) {
;             const bool last = (t == nt - 2);
;             const char* a1 = cA + (size_t)(t + 1) * kstep;
;             const char* a2 = last ? nA : cA + (size_t)(t + 2) * kstep; const char* b2 = last ? nB : cB + (size_t)(t + 2) * kstep;
;             const char* a3 = a2 + kstep; const char* b3 = b2 + kstep;
;             if (last && has_next) S.a_ready(nxt);
;             if constexpr (SP2) {
;             PG8_LDB(B0, 0, 0); PG8_LDB(B1, 0, 1); PG8_SCHED; PG8_LDA(At, 0, 0); PG8_STAGE_A(PG8_SA(1, 1), a1, 1, false);
;             PG8_WAIT_V(8); PG8_WAIT_L(0); PG8_BAR; PG8_MMA(0, 0, At, B0); PG8_MMA(0, 1, At, B1); PG8_BAR; PG8_SCHED;
;             PG8_LDA(At, 0, 1); PG8_STAGE(PG8_SB(0, 0), b2, voffB); PG8_STAGE(PG8_SB(0, 1), b2 + hstepB, voffB); PG8_STAGE_A(PG8_SA(0, 0), a2, 0, last);
;             PG8_WAIT_V(8); PG8_WAIT_L(0); PG8_BAR; PG8_MMA(1, 0, At, B0); PG8_MMA(1, 1, At, B1); PG8_BAR; PG8_SCHED;
.LBB0_153:
	ds_read_b128 v[26:29], v205
	ds_read_b128 v[30:33], v205 offset:1024
	ds_read_b128 v[18:21], v205 offset:2048
	ds_read_b128 v[22:25], v205 offset:3072
	ds_read_b128 v[10:13], v206
	ds_read_b128 v[14:17], v206 offset:1024
	ds_read_b128 v[2:5], v206 offset:2048
	ds_read_b128 v[6:9], v206 offset:3072
	s_add_u32 s10, s8, 0xfffe0080
	s_addc_u32 s11, s9, -1
	s_cmp_eq_u32 s33, 4
	s_cselect_b32 s67, s0, s11
	s_cselect_b32 s66, s1, s10
	s_cselect_b32 s11, s5, s19
	s_cselect_b32 s10, s7, s18
	v_lshl_add_u64 v[162:163], s[8:9], 0, v[176:177]
	s_add_i32 m0, s82, 0xc000
	ds_read_b128 v[184:187], v207
	ds_read_b128 v[188:191], v207 offset:1024
	ds_read_b128 v[192:195], v207 offset:2048
	ds_read_b128 v[196:199], v207 offset:3072
	ds_read_b128 v[214:217], v207 offset:4096
	ds_read_b128 v[218:221], v207 offset:5120
	ds_read_b128 v[222:225], v207 offset:6144
	ds_read_b128 v[226:229], v207 offset:7168
	global_load_lds_dwordx4 v[162:163], off
	v_lshl_add_u64 v[162:163], s[8:9], 0, v[178:179]
	s_add_i32 m0, s82, 0xe000
	s_nop 0
	global_load_lds_dwordx4 v[162:163], off
	s_waitcnt vmcnt(8)
	s_waitcnt lgkmcnt(0)
	s_barrier
	s_setprio 1
	s_nop 3
	s_waitcnt lgkmcnt(0)
	v_mfma_scale_f32_16x16x128_f8f6f4 v[158:161], v[26:33], v[184:191], v[158:161], v208, v209 op_sel_hi:[0,0,0]
	v_mfma_scale_f32_16x16x128_f8f6f4 v[154:157], v[18:25], v[184:191], v[154:157], v208, v209 op_sel_hi:[0,0,0]
	v_mfma_scale_f32_16x16x128_f8f6f4 v[142:145], v[26:33], v[192:199], v[142:145], v208, v209 op_sel_hi:[0,0,0]
	v_mfma_scale_f32_16x16x128_f8f6f4 v[138:141], v[18:25], v[192:199], v[138:141], v208, v209 op_sel_hi:[0,0,0]
	v_mfma_scale_f32_16x16x128_f8f6f4 v[126:129], v[26:33], v[214:221], v[126:129], v208, v209 op_sel_hi:[0,0,0]
	v_mfma_scale_f32_16x16x128_f8f6f4 v[122:125], v[18:25], v[214:221], v[122:125], v208, v209 op_sel_hi:[0,0,0]
	v_mfma_scale_f32_16x16x128_f8f6f4 v[110:113], v[26:33], v[222:229], v[110:113], v208, v209 op_sel_hi:[0,0,0]
	v_mfma_scale_f32_16x16x128_f8f6f4 v[106:109], v[18:25], v[222:229], v[106:109], v208, v209 op_sel_hi:[0,0,0]
	s_setprio 0
	s_setprio 1
	s_nop 3
	v_mfma_scale_f32_16x16x128_f8f6f4 v[150:153], v[10:17], v[184:191], v[150:153], v208, v209 op_sel_hi:[0,0,0]
	v_mfma_scale_f32_16x16x128_f8f6f4 v[146:149], v[2:9], v[184:191], v[146:149], v208, v209 op_sel_hi:[0,0,0]
	v_mfma_scale_f32_16x16x128_f8f6f4 v[134:137], v[10:17], v[192:199], v[134:137], v208, v209 op_sel_hi:[0,0,0]
	v_mfma_scale_f32_16x16x128_f8f6f4 v[130:133], v[2:9], v[192:199], v[130:133], v208, v209 op_sel_hi:[0,0,0]
	v_mfma_scale_f32_16x16x128_f8f6f4 v[118:121], v[10:17], v[214:221], v[118:121], v208, v209 op_sel_hi:[0,0,0]
	v_mfma_scale_f32_16x16x128_f8f6f4 v[114:117], v[2:9], v[214:221], v[114:117], v208, v209 op_sel_hi:[0,0,0]
	v_mfma_scale_f32_16x16x128_f8f6f4 v[102:105], v[10:17], v[222:229], v[102:105], v208, v209 op_sel_hi:[0,0,0]
	v_mfma_scale_f32_16x16x128_f8f6f4 v[98:101], v[2:9], v[222:229], v[98:101], v208, v209 op_sel_hi:[0,0,0]
	s_setprio 0
	s_barrier
	s_add_i32 s59, s96, s77
	v_lshl_add_u64 v[162:163], s[10:11], 0, v[168:169]
	s_mov_b32 m0, s59
	ds_read_b128 v[188:191], v207 offset:16384
	ds_read_b128 v[192:195], v207 offset:17408
	ds_read_b128 v[214:217], v207 offset:18432
	ds_read_b128 v[218:221], v207 offset:19456
	ds_read_b128 v[222:225], v207 offset:20480
	ds_read_b128 v[226:229], v207 offset:21504
	ds_read_b128 v[230:233], v207 offset:22528
	ds_read_b128 v[234:237], v207 offset:23552
	global_load_lds_dwordx4 v[162:163], off
	s_add_i32 m0, s59, 0x2000
	s_add_u32 s68, s10, 0x8000
	v_lshl_add_u64 v[164:165], s[10:11], 0, v[172:173]
	s_addc_u32 s69, s11, 0
	s_add_i32 s59, s97, s77
	global_load_lds_dwordx4 v[164:165], off
	v_lshl_add_u64 v[184:185], s[68:69], 0, v[168:169]
	s_mov_b32 m0, s59
	v_lshl_add_u64 v[186:187], s[66:67], 0, v[170:171]
	global_load_lds_dwordx4 v[184:185], off
	v_lshl_add_u64 v[184:185], s[68:69], 0, v[172:173]
	s_add_i32 m0, s59, 0x2000
	s_nop 0
	global_load_lds_dwordx4 v[184:185], off
	v_lshl_add_u64 v[184:185], s[66:67], 0, v[166:167]
	s_mov_b32 m0, s82
	s_nop 0
	global_load_lds_dwordx4 v[184:185], off
	s_mov_b32 m0, s83
	s_nop 0
	global_load_lds_dwordx4 v[186:187], off
	s_waitcnt vmcnt(8)
	s_waitcnt lgkmcnt(0)
	s_barrier
	s_setprio 1
	s_nop 3
	s_waitcnt lgkmcnt(0)
	v_mfma_scale_f32_16x16x128_f8f6f4 v[94:97], v[26:33], v[188:195], v[94:97], v208, v209 op_sel_hi:[0,0,0]
	v_mfma_scale_f32_16x16x128_f8f6f4 v[90:93], v[18:25], v[188:195], v[90:93], v208, v209 op_sel_hi:[0,0,0]
	v_mfma_scale_f32_16x16x128_f8f6f4 v[78:81], v[26:33], v[214:221], v[78:81], v208, v209 op_sel_hi:[0,0,0]
	v_mfma_scale_f32_16x16x128_f8f6f4 v[74:77], v[18:25], v[214:221], v[74:77], v208, v209 op_sel_hi:[0,0,0]
	v_mfma_scale_f32_16x16x128_f8f6f4 v[62:65], v[26:33], v[222:229], v[62:65], v208, v209 op_sel_hi:[0,0,0]
	v_mfma_scale_f32_16x16x128_f8f6f4 v[58:61], v[18:25], v[222:229], v[58:61], v208, v209 op_sel_hi:[0,0,0]
	v_mfma_scale_f32_16x16x128_f8f6f4 v[46:49], v[26:33], v[230:237], v[46:49], v208, v209 op_sel_hi:[0,0,0]
	v_mfma_scale_f32_16x16x128_f8f6f4 v[42:45], v[18:25], v[230:237], v[42:45], v208, v209 op_sel_hi:[0,0,0]
	s_setprio 0
	s_setprio 1
	s_nop 3
	v_mfma_scale_f32_16x16x128_f8f6f4 v[86:89], v[10:17], v[188:195], v[86:89], v208, v209 op_sel_hi:[0,0,0]
	v_mfma_scale_f32_16x16x128_f8f6f4 v[82:85], v[2:9], v[188:195], v[82:85], v208, v209 op_sel_hi:[0,0,0]
	v_mfma_scale_f32_16x16x128_f8f6f4 v[70:73], v[10:17], v[214:221], v[70:73], v208, v209 op_sel_hi:[0,0,0]
	v_mfma_scale_f32_16x16x128_f8f6f4 v[66:69], v[2:9], v[214:221], v[66:69], v208, v209 op_sel_hi:[0,0,0]
	v_mfma_scale_f32_16x16x128_f8f6f4 v[54:57], v[10:17], v[222:229], v[54:57], v208, v209 op_sel_hi:[0,0,0]
	v_mfma_scale_f32_16x16x128_f8f6f4 v[50:53], v[2:9], v[222:229], v[50:53], v208, v209 op_sel_hi:[0,0,0]
	v_mfma_scale_f32_16x16x128_f8f6f4 v[38:41], v[10:17], v[230:237], v[38:41], v208, v209 op_sel_hi:[0,0,0]
	v_mfma_scale_f32_16x16x128_f8f6f4 v[34:37], v[2:9], v[230:237], v[34:37], v208, v209 op_sel_hi:[0,0,0]
	s_setprio 0
	s_barrier
; #define PG8_STAGE(bufoff, gbase, voff) do { _Pragma("unroll") for (int _i = 0; _i < 2; ++_i) \
;         __builtin_amdgcn_global_load_lds((const unsigned*)((const char*)(gbase) + (voff)[_i]), (PG8_LAS unsigned*)(lds + (bufoff) + ldsw + _i * 8192), 16, 0, 0); } while (0)
; #define PG8_STAGE_A(bufoff, gbase, h, nx) do { if constexpr (Sched::GATHER) { const unsigned vv_[2] = {(nx) ? vAn[h][0] : vA[h][0], (nx) ? vAn[h][1] : vA[h][1]}; PG8_STAGE(bufoff, gbase, vv_); } \
;         else { PG8_STAGE(bufoff, (gbase) + (h) * hstep, voffA); } } while (0)
; #define PG8_LDA(dst, b, h) do { _Pragma("unroll") for (int m = 0; m < 4; ++m) _Pragma("unroll") for (int k = 0; k < 2; ++k) dst[m][k] = *(const PG8_LAS bf16x8*)(lds + PG8_SA(b, h) + aoff + m * 2048 + k * 1024); } while (0)
; #define PG8_LDB(dst, b, h) do { _Pragma("unroll") for (int n = 0; n < 2; ++n) _Pragma("unroll") for (int k = 0; k < 2; ++k) dst[n][k] = *(const PG8_LAS bf16x8*)(lds + PG8_SB(b, h) + boff + n * 2048 + k * 1024); } while (0)
; #define PG8_WAIT_V(n) asm volatile("s_waitcnt vmcnt(" #n ")" ::: "memory")
; #define PG8_WAIT_L(n) asm volatile("s_waitcnt lgkmcnt(" #n ")" ::: "memory")
; #define PG8_BAR __builtin_amdgcn_s_barrier()
; #define PG8_SCHED __builtin_amdgcn_sched_barrier(0)
;     ...
;         for (int t = 0; t < nt; t += 2) {
;     ...
;             PG8_LDB(B0, 1, 0); PG8_LDB(B1, 1, 1); PG8_SCHED; PG8_LDA(At, 1, 0); PG8_STAGE_A(PG8_SA(0, 1), a2, 1, last);
;             PG8_WAIT_V(8); PG8_WAIT_L(0); PG8_BAR; PG8_MMA(0, 0, At, B0); PG8_MMA(0, 1, At, B1); PG8_BAR; PG8_SCHED;
;             PG8_LDA(At, 1, 1); PG8_STAGE(PG8_SB(1, 0), b3, voffB); PG8_STAGE(PG8_SB(1, 1), b3 + hstepB, voffB); PG8_STAGE_A(PG8_SA(1, 0), a3, 0, last);
;             PG8_WAIT_V(8); PG8_WAIT_L(0); PG8_BAR; PG8_MMA(1, 0, At, B0); PG8_MMA(1, 1, At, B1); PG8_BAR; PG8_SCHED;
	s_add_i32 s59, 0, 0x18000
	s_add_i32 s61, 0, 0x1c000
	v_add_u32_e32 v14, s59, v203
	v_add_u32_e32 v30, s61, v203
	ds_read_b128 v[2:5], v14
	ds_read_b128 v[6:9], v14 offset:1024
	ds_read_b128 v[10:13], v14 offset:2048
	ds_read_b128 v[14:17], v14 offset:3072
	ds_read_b128 v[18:21], v30
	ds_read_b128 v[22:25], v30 offset:1024
	ds_read_b128 v[26:29], v30 offset:2048
	ds_read_b128 v[30:33], v30 offset:3072
	s_add_u32 s66, s66, 0x20000
	s_addc_u32 s67, s67, 0
	s_mov_b32 m0, s84
	v_lshl_add_u64 v[196:197], s[66:67], 0, v[166:167]
	ds_read_b128 v[188:191], v207 offset:32768
	ds_read_b128 v[192:195], v207 offset:33792
	ds_read_b128 v[214:217], v207 offset:34816
	ds_read_b128 v[218:221], v207 offset:35840
	ds_read_b128 v[222:225], v207 offset:36864
	ds_read_b128 v[226:229], v207 offset:37888
	ds_read_b128 v[230:233], v207 offset:38912
	ds_read_b128 v[234:237], v207 offset:39936
	global_load_lds_dwordx4 v[196:197], off
	v_lshl_add_u64 v[196:197], s[66:67], 0, v[170:171]
	s_mov_b32 m0, s85
	s_nop 0
	global_load_lds_dwordx4 v[196:197], off
	s_waitcnt vmcnt(8)
	s_waitcnt lgkmcnt(0)
	s_barrier
	s_setprio 1
	s_nop 3
	s_waitcnt lgkmcnt(0)
	v_mfma_scale_f32_16x16x128_f8f6f4 v[158:161], v[2:9], v[188:195], v[158:161], v208, v209 op_sel_hi:[0,0,0]
	v_mfma_scale_f32_16x16x128_f8f6f4 v[154:157], v[10:17], v[188:195], v[154:157], v208, v209 op_sel_hi:[0,0,0]
	v_mfma_scale_f32_16x16x128_f8f6f4 v[142:145], v[2:9], v[214:221], v[142:145], v208, v209 op_sel_hi:[0,0,0]
	v_mfma_scale_f32_16x16x128_f8f6f4 v[138:141], v[10:17], v[214:221], v[138:141], v208, v209 op_sel_hi:[0,0,0]
	v_mfma_scale_f32_16x16x128_f8f6f4 v[126:129], v[2:9], v[222:229], v[126:129], v208, v209 op_sel_hi:[0,0,0]
	v_mfma_scale_f32_16x16x128_f8f6f4 v[122:125], v[10:17], v[222:229], v[122:125], v208, v209 op_sel_hi:[0,0,0]
	v_mfma_scale_f32_16x16x128_f8f6f4 v[110:113], v[2:9], v[230:237], v[110:113], v208, v209 op_sel_hi:[0,0,0]
	v_mfma_scale_f32_16x16x128_f8f6f4 v[106:109], v[10:17], v[230:237], v[106:109], v208, v209 op_sel_hi:[0,0,0]
	s_setprio 0
	s_setprio 1
	s_nop 3
	v_mfma_scale_f32_16x16x128_f8f6f4 v[150:153], v[18:25], v[188:195], v[150:153], v208, v209 op_sel_hi:[0,0,0]
	v_mfma_scale_f32_16x16x128_f8f6f4 v[146:149], v[26:33], v[188:195], v[146:149], v208, v209 op_sel_hi:[0,0,0]
	v_mfma_scale_f32_16x16x128_f8f6f4 v[134:137], v[18:25], v[214:221], v[134:137], v208, v209 op_sel_hi:[0,0,0]
	v_mfma_scale_f32_16x16x128_f8f6f4 v[130:133], v[26:33], v[214:221], v[130:133], v208, v209 op_sel_hi:[0,0,0]
	v_mfma_scale_f32_16x16x128_f8f6f4 v[118:121], v[18:25], v[222:229], v[118:121], v208, v209 op_sel_hi:[0,0,0]
	v_mfma_scale_f32_16x16x128_f8f6f4 v[114:117], v[26:33], v[222:229], v[114:117], v208, v209 op_sel_hi:[0,0,0]
	v_mfma_scale_f32_16x16x128_f8f6f4 v[102:105], v[18:25], v[230:237], v[102:105], v208, v209 op_sel_hi:[0,0,0]
	v_mfma_scale_f32_16x16x128_f8f6f4 v[98:101], v[26:33], v[230:237], v[98:101], v208, v209 op_sel_hi:[0,0,0]
	s_setprio 0
	s_barrier
	s_add_i32 s59, s59, s77
	v_lshl_add_u64 v[162:163], v[162:163], 0, s[40:41]
	s_mov_b32 m0, s59
	ds_read_b128 v[188:191], v207 offset:49152
	ds_read_b128 v[192:195], v207 offset:50176
	ds_read_b128 v[214:217], v207 offset:51200
	ds_read_b128 v[218:221], v207 offset:52224
	ds_read_b128 v[222:225], v207 offset:53248
	ds_read_b128 v[226:229], v207 offset:54272
	ds_read_b128 v[230:233], v207 offset:55296
	ds_read_b128 v[234:237], v207 offset:56320
	global_load_lds_dwordx4 v[162:163], off
	s_add_i32 m0, s59, 0x2000
	s_add_u32 s10, s10, 0x8080
	v_lshl_add_u64 v[162:163], v[164:165], 0, s[40:41]
	s_addc_u32 s11, s11, 0
	s_add_i32 s59, s61, s77
	global_load_lds_dwordx4 v[162:163], off
	v_lshl_add_u64 v[162:163], s[10:11], 0, v[168:169]
	s_mov_b32 m0, s59
	s_nop 0
	global_load_lds_dwordx4 v[162:163], off
	v_lshl_add_u64 v[162:163], s[10:11], 0, v[172:173]
	s_add_i32 m0, s59, 0x2000
	s_nop 0
	global_load_lds_dwordx4 v[162:163], off
	v_lshl_add_u64 v[162:163], v[184:185], 0, s[40:41]
	s_mov_b32 m0, s94
	s_nop 0
	global_load_lds_dwordx4 v[162:163], off
	v_lshl_add_u64 v[162:163], v[186:187], 0, s[40:41]
	s_mov_b32 m0, s95
	s_nop 0
	global_load_lds_dwordx4 v[162:163], off
	s_waitcnt vmcnt(8)
	s_waitcnt lgkmcnt(0)
	s_barrier
	s_setprio 1
	s_nop 3
	s_waitcnt lgkmcnt(0)
	v_mfma_scale_f32_16x16x128_f8f6f4 v[94:97], v[2:9], v[188:195], v[94:97], v208, v209 op_sel_hi:[0,0,0]
	v_mfma_scale_f32_16x16x128_f8f6f4 v[90:93], v[10:17], v[188:195], v[90:93], v208, v209 op_sel_hi:[0,0,0]
	v_mfma_scale_f32_16x16x128_f8f6f4 v[78:81], v[2:9], v[214:221], v[78:81], v208, v209 op_sel_hi:[0,0,0]
	v_mfma_scale_f32_16x16x128_f8f6f4 v[74:77], v[10:17], v[214:221], v[74:77], v208, v209 op_sel_hi:[0,0,0]
	v_mfma_scale_f32_16x16x128_f8f6f4 v[62:65], v[2:9], v[222:229], v[62:65], v208, v209 op_sel_hi:[0,0,0]
	v_mfma_scale_f32_16x16x128_f8f6f4 v[58:61], v[10:17], v[222:229], v[58:61], v208, v209 op_sel_hi:[0,0,0]
	v_mfma_scale_f32_16x16x128_f8f6f4 v[46:49], v[2:9], v[230:237], v[46:49], v208, v209 op_sel_hi:[0,0,0]
	v_mfma_scale_f32_16x16x128_f8f6f4 v[42:45], v[10:17], v[230:237], v[42:45], v208, v209 op_sel_hi:[0,0,0]
	s_setprio 0
	s_setprio 1
	s_nop 3
	v_mfma_scale_f32_16x16x128_f8f6f4 v[86:89], v[18:25], v[188:195], v[86:89], v208, v209 op_sel_hi:[0,0,0]
	v_mfma_scale_f32_16x16x128_f8f6f4 v[82:85], v[26:33], v[188:195], v[82:85], v208, v209 op_sel_hi:[0,0,0]
	v_mfma_scale_f32_16x16x128_f8f6f4 v[70:73], v[18:25], v[214:221], v[70:73], v208, v209 op_sel_hi:[0,0,0]
	v_mfma_scale_f32_16x16x128_f8f6f4 v[66:69], v[26:33], v[214:221], v[66:69], v208, v209 op_sel_hi:[0,0,0]
	v_mfma_scale_f32_16x16x128_f8f6f4 v[54:57], v[18:25], v[222:229], v[54:57], v208, v209 op_sel_hi:[0,0,0]
	v_mfma_scale_f32_16x16x128_f8f6f4 v[50:53], v[26:33], v[222:229], v[50:53], v208, v209 op_sel_hi:[0,0,0]
	v_mfma_scale_f32_16x16x128_f8f6f4 v[38:41], v[18:25], v[230:237], v[38:41], v208, v209 op_sel_hi:[0,0,0]
	v_mfma_scale_f32_16x16x128_f8f6f4 v[34:37], v[26:33], v[230:237], v[34:37], v208, v209 op_sel_hi:[0,0,0]
	s_setprio 0
	s_add_i32 s33, s33, 2
	s_add_u32 s8, s8, 0x100
	s_addc_u32 s9, s9, 0
	s_add_u32 s18, s18, 0x100
	s_addc_u32 s19, s19, 0
	s_cmp_gt_u32 s33, 5
	s_barrier
	s_cbranch_scc0 .LBB0_153
	s_and_b64 vcc, exec, s[42:43]
	s_cbranch_vccz .LBB0_156
	s_barrier

; #define PG8_STAGE(bufoff, gbase, voff) do { _Pragma("unroll") for (int _i = 0; _i < 2; ++_i) \
;         __builtin_amdgcn_global_load_lds((const unsigned*)((const char*)(gbase) + (voff)[_i]), (PG8_LAS unsigned*)(lds + (bufoff) + ldsw + _i * 8192), 16, 0, 0); } while (0)
; #define PG8_STAGE_A(bufoff, gbase, h, nx) do { if constexpr (Sched::GATHER) { const unsigned vv_[2] = {(nx) ? vAn[h][0] : vA[h][0], (nx) ? vAn[h][1] : vA[h][1]}; PG8_STAGE(bufoff, gbase, vv_); } \
;         else { PG8_STAGE(bufoff, (gbase) + (h) * hstep, voffA); } } while (0)
; #define PG8_LDA(dst, b, h) do { _Pragma("unroll") for (int m = 0; m < 4; ++m) _Pragma("unroll") for (int k = 0; k < 2; ++k) dst[m][k] = *(const PG8_LAS bf16x8*)(lds + PG8_SA(b, h) + aoff + m * 2048 + k * 1024); } while (0)
; #define PG8_LDB(dst, b, h) do { _Pragma("unroll") for (int n = 0; n < 2; ++n) _Pragma("unroll") for (int k = 0; k < 2; ++k) dst[n][k] = *(const PG8_LAS bf16x8*)(lds + PG8_SB(b, h) + boff + n * 2048 + k * 1024); } while (0)
; #define PG8_WAIT_V(n) asm volatile("s_waitcnt vmcnt(" #n ")" ::: "memory")
; #define PG8_WAIT_L(n) asm volatile("s_waitcnt lgkmcnt(" #n ")" ::: "memory")
; #define PG8_BAR __builtin_amdgcn_s_barrier()
; #define PG8_SCHED __builtin_amdgcn_sched_barrier(0)
;     ...
;         for (int t = 0; t < nt; t += 2) {
;             const bool last = (t == nt - 2);
;             const char* a1 = cA + (size_t)(t + 1) * kstep;
;             const char* a2 = last ? nA : cA + (size_t)(t + 2) * kstep; const char* b2 = last ? nB : cB + (size_t)(t + 2) * kstep;
;             const char* a3 = a2 + kstep; const char* b3 = b2 + kstep;
;             if (last && has_next) S.a_ready(nxt);
;             if constexpr (SP2) {
;             PG8_LDB(B0, 0, 0); PG8_LDB(B1, 0, 1); PG8_SCHED; PG8_LDA(At, 0, 0); PG8_STAGE_A(PG8_SA(1, 1), a1, 1, false);
;             PG8_WAIT_V(8); PG8_WAIT_L(0); PG8_BAR; PG8_MMA(0, 0, At, B0); PG8_MMA(0, 1, At, B1); PG8_BAR; PG8_SCHED;
;             PG8_LDA(At, 0, 1); PG8_STAGE(PG8_SB(0, 0), b2, voffB); PG8_STAGE(PG8_SB(0, 1), b2 + hstepB, voffB); PG8_STAGE_A(PG8_SA(0, 0), a2, 0, last);
;             PG8_WAIT_V(8); PG8_WAIT_L(0); PG8_BAR; PG8_MMA(1, 0, At, B0); PG8_MMA(1, 1, At, B1); PG8_BAR; PG8_SCHED;
.LBB0_474:
	ds_read_b128 v[26:29], v188
	ds_read_b128 v[30:33], v188 offset:1024
	ds_read_b128 v[18:21], v188 offset:2048
	ds_read_b128 v[22:25], v188 offset:3072
	ds_read_b128 v[10:13], v189
	ds_read_b128 v[14:17], v189 offset:1024
	ds_read_b128 v[2:5], v189 offset:2048
	ds_read_b128 v[6:9], v189 offset:3072
	s_add_u32 s24, s22, 0xfffe0080
	s_addc_u32 s25, s23, -1
	s_cmp_eq_u32 s43, 4
	s_cselect_b32 s27, s1, s25
	s_cselect_b32 s26, s15, s24
	s_cselect_b32 s25, s13, s42
	s_cselect_b32 s24, s21, s33
	v_lshl_add_u64 v[218:219], s[22:23], 0, v[170:171]
	s_add_i32 m0, s30, 0xc000
	ds_read_b128 v[178:181], v190
	ds_read_b128 v[182:185], v190 offset:1024
	ds_read_b128 v[194:197], v190 offset:2048
	ds_read_b128 v[198:201], v190 offset:3072
	ds_read_b128 v[202:205], v190 offset:4096
	ds_read_b128 v[206:209], v190 offset:5120
	ds_read_b128 v[210:213], v190 offset:6144
	ds_read_b128 v[214:217], v190 offset:7168
	global_load_lds_dwordx4 v[218:219], off
	v_lshl_add_u64 v[218:219], s[22:23], 0, v[172:173]
	s_add_i32 m0, s30, 0xe000
	s_nop 0
	global_load_lds_dwordx4 v[218:219], off
	s_waitcnt vmcnt(8)
	s_waitcnt lgkmcnt(0)
	s_barrier
	s_setprio 1
	s_nop 3
	s_waitcnt lgkmcnt(0)
	v_mfma_scale_f32_16x16x128_f8f6f4 v[158:161], v[26:33], v[178:185], v[158:161], v191, v192 op_sel_hi:[0,0,0]
	v_mfma_scale_f32_16x16x128_f8f6f4 v[154:157], v[18:25], v[178:185], v[154:157], v191, v192 op_sel_hi:[0,0,0]
	v_mfma_scale_f32_16x16x128_f8f6f4 v[142:145], v[26:33], v[194:201], v[142:145], v191, v192 op_sel_hi:[0,0,0]
	v_mfma_scale_f32_16x16x128_f8f6f4 v[138:141], v[18:25], v[194:201], v[138:141], v191, v192 op_sel_hi:[0,0,0]
	v_mfma_scale_f32_16x16x128_f8f6f4 v[126:129], v[26:33], v[202:209], v[126:129], v191, v192 op_sel_hi:[0,0,0]
	v_mfma_scale_f32_16x16x128_f8f6f4 v[122:125], v[18:25], v[202:209], v[122:125], v191, v192 op_sel_hi:[0,0,0]
	v_mfma_scale_f32_16x16x128_f8f6f4 v[110:113], v[26:33], v[210:217], v[110:113], v191, v192 op_sel_hi:[0,0,0]
	v_mfma_scale_f32_16x16x128_f8f6f4 v[106:109], v[18:25], v[210:217], v[106:109], v191, v192 op_sel_hi:[0,0,0]
	s_setprio 0
	s_setprio 1
	s_nop 3
	v_mfma_scale_f32_16x16x128_f8f6f4 v[150:153], v[10:17], v[178:185], v[150:153], v191, v192 op_sel_hi:[0,0,0]
	v_mfma_scale_f32_16x16x128_f8f6f4 v[146:149], v[2:9], v[178:185], v[146:149], v191, v192 op_sel_hi:[0,0,0]
	v_mfma_scale_f32_16x16x128_f8f6f4 v[134:137], v[10:17], v[194:201], v[134:137], v191, v192 op_sel_hi:[0,0,0]
	v_mfma_scale_f32_16x16x128_f8f6f4 v[130:133], v[2:9], v[194:201], v[130:133], v191, v192 op_sel_hi:[0,0,0]
	v_mfma_scale_f32_16x16x128_f8f6f4 v[118:121], v[10:17], v[202:209], v[118:121], v191, v192 op_sel_hi:[0,0,0]
	v_mfma_scale_f32_16x16x128_f8f6f4 v[114:117], v[2:9], v[202:209], v[114:117], v191, v192 op_sel_hi:[0,0,0]
	v_mfma_scale_f32_16x16x128_f8f6f4 v[102:105], v[10:17], v[210:217], v[102:105], v191, v192 op_sel_hi:[0,0,0]
	v_mfma_scale_f32_16x16x128_f8f6f4 v[98:101], v[2:9], v[210:217], v[98:101], v191, v192 op_sel_hi:[0,0,0]
	s_setprio 0
	s_barrier
	s_add_i32 s44, s40, s28
	v_lshl_add_u64 v[178:179], s[24:25], 0, v[164:165]
	s_mov_b32 m0, s44
	ds_read_b128 v[194:197], v190 offset:16384
	ds_read_b128 v[198:201], v190 offset:17408
	ds_read_b128 v[202:205], v190 offset:18432
	ds_read_b128 v[206:209], v190 offset:19456
	ds_read_b128 v[210:213], v190 offset:20480
	ds_read_b128 v[214:217], v190 offset:21504
	ds_read_b128 v[218:221], v190 offset:22528
	ds_read_b128 v[222:225], v190 offset:23552
	global_load_lds_dwordx4 v[178:179], off
	s_add_i32 m0, s44, 0x2000
	s_add_u32 s44, s24, 0x2000
	v_lshl_add_u64 v[180:181], s[24:25], 0, v[168:169]
	s_addc_u32 s45, s25, 0
	s_add_i32 s46, s41, s28
	global_load_lds_dwordx4 v[180:181], off
	v_lshl_add_u64 v[182:183], s[44:45], 0, v[164:165]
	s_mov_b32 m0, s46
	v_lshl_add_u64 v[184:185], s[26:27], 0, v[166:167]
	global_load_lds_dwordx4 v[182:183], off
	v_lshl_add_u64 v[182:183], s[44:45], 0, v[168:169]
	s_add_i32 m0, s46, 0x2000
	s_nop 0
	global_load_lds_dwordx4 v[182:183], off
	v_lshl_add_u64 v[182:183], s[26:27], 0, v[162:163]
	s_mov_b32 m0, s30
	s_nop 0
	global_load_lds_dwordx4 v[182:183], off
	s_mov_b32 m0, s31
	s_nop 0
	global_load_lds_dwordx4 v[184:185], off
	s_waitcnt vmcnt(8)
	s_waitcnt lgkmcnt(0)
	s_barrier
	s_setprio 1
	s_nop 3
	s_waitcnt lgkmcnt(0)
	v_mfma_scale_f32_16x16x128_f8f6f4 v[94:97], v[26:33], v[194:201], v[94:97], v191, v192 op_sel_hi:[0,0,0]
	v_mfma_scale_f32_16x16x128_f8f6f4 v[90:93], v[18:25], v[194:201], v[90:93], v191, v192 op_sel_hi:[0,0,0]
	v_mfma_scale_f32_16x16x128_f8f6f4 v[78:81], v[26:33], v[202:209], v[78:81], v191, v192 op_sel_hi:[0,0,0]
	v_mfma_scale_f32_16x16x128_f8f6f4 v[74:77], v[18:25], v[202:209], v[74:77], v191, v192 op_sel_hi:[0,0,0]
	v_mfma_scale_f32_16x16x128_f8f6f4 v[62:65], v[26:33], v[210:217], v[62:65], v191, v192 op_sel_hi:[0,0,0]
	v_mfma_scale_f32_16x16x128_f8f6f4 v[58:61], v[18:25], v[210:217], v[58:61], v191, v192 op_sel_hi:[0,0,0]
	v_mfma_scale_f32_16x16x128_f8f6f4 v[46:49], v[26:33], v[218:225], v[46:49], v191, v192 op_sel_hi:[0,0,0]
	v_mfma_scale_f32_16x16x128_f8f6f4 v[42:45], v[18:25], v[218:225], v[42:45], v191, v192 op_sel_hi:[0,0,0]
	s_setprio 0
	s_setprio 1
	s_nop 3
	v_mfma_scale_f32_16x16x128_f8f6f4 v[86:89], v[10:17], v[194:201], v[86:89], v191, v192 op_sel_hi:[0,0,0]
	v_mfma_scale_f32_16x16x128_f8f6f4 v[82:85], v[2:9], v[194:201], v[82:85], v191, v192 op_sel_hi:[0,0,0]
	v_mfma_scale_f32_16x16x128_f8f6f4 v[70:73], v[10:17], v[202:209], v[70:73], v191, v192 op_sel_hi:[0,0,0]
	v_mfma_scale_f32_16x16x128_f8f6f4 v[66:69], v[2:9], v[202:209], v[66:69], v191, v192 op_sel_hi:[0,0,0]
	v_mfma_scale_f32_16x16x128_f8f6f4 v[54:57], v[10:17], v[210:217], v[54:57], v191, v192 op_sel_hi:[0,0,0]
	v_mfma_scale_f32_16x16x128_f8f6f4 v[50:53], v[2:9], v[210:217], v[50:53], v191, v192 op_sel_hi:[0,0,0]
	v_mfma_scale_f32_16x16x128_f8f6f4 v[38:41], v[10:17], v[218:225], v[38:41], v191, v192 op_sel_hi:[0,0,0]
	v_mfma_scale_f32_16x16x128_f8f6f4 v[34:37], v[2:9], v[218:225], v[34:37], v191, v192 op_sel_hi:[0,0,0]
	s_setprio 0
	s_barrier
; #define PG8_STAGE(bufoff, gbase, voff) do { _Pragma("unroll") for (int _i = 0; _i < 2; ++_i) \
;         __builtin_amdgcn_global_load_lds((const unsigned*)((const char*)(gbase) + (voff)[_i]), (PG8_LAS unsigned*)(lds + (bufoff) + ldsw + _i * 8192), 16, 0, 0); } while (0)
; #define PG8_STAGE_A(bufoff, gbase, h, nx) do { if constexpr (Sched::GATHER) { const unsigned vv_[2] = {(nx) ? vAn[h][0] : vA[h][0], (nx) ? vAn[h][1] : vA[h][1]}; PG8_STAGE(bufoff, gbase, vv_); } \
;         else { PG8_STAGE(bufoff, (gbase) + (h) * hstep, voffA); } } while (0)
; #define PG8_LDA(dst, b, h) do { _Pragma("unroll") for (int m = 0; m < 4; ++m) _Pragma("unroll") for (int k = 0; k < 2; ++k) dst[m][k] = *(const PG8_LAS bf16x8*)(lds + PG8_SA(b, h) + aoff + m * 2048 + k * 1024); } while (0)
; #define PG8_LDB(dst, b, h) do { _Pragma("unroll") for (int n = 0; n < 2; ++n) _Pragma("unroll") for (int k = 0; k < 2; ++k) dst[n][k] = *(const PG8_LAS bf16x8*)(lds + PG8_SB(b, h) + boff + n * 2048 + k * 1024); } while (0)
; #define PG8_WAIT_V(n) asm volatile("s_waitcnt vmcnt(" #n ")" ::: "memory")
; #define PG8_WAIT_L(n) asm volatile("s_waitcnt lgkmcnt(" #n ")" ::: "memory")
; #define PG8_BAR __builtin_amdgcn_s_barrier()
; #define PG8_SCHED __builtin_amdgcn_sched_barrier(0)
;     ...
;         for (int t = 0; t < nt; t += 2) {
;     ...
;             PG8_LDB(B0, 1, 0); PG8_LDB(B1, 1, 1); PG8_SCHED; PG8_LDA(At, 1, 0); PG8_STAGE_A(PG8_SA(0, 1), a2, 1, last);
;             PG8_WAIT_V(8); PG8_WAIT_L(0); PG8_BAR; PG8_MMA(0, 0, At, B0); PG8_MMA(0, 1, At, B1); PG8_BAR; PG8_SCHED;
;             PG8_LDA(At, 1, 1); PG8_STAGE(PG8_SB(1, 0), b3, voffB); PG8_STAGE(PG8_SB(1, 1), b3 + hstepB, voffB); PG8_STAGE_A(PG8_SA(1, 0), a3, 0, last);
;             PG8_WAIT_V(8); PG8_WAIT_L(0); PG8_BAR; PG8_MMA(1, 0, At, B0); PG8_MMA(1, 1, At, B1); PG8_BAR; PG8_SCHED;
	s_add_i32 s44, 0, 0x18000
	s_add_i32 s45, 0, 0x1c000
	v_add_u32_e32 v14, s44, v186
	v_add_u32_e32 v30, s45, v186
	ds_read_b128 v[2:5], v14
	ds_read_b128 v[6:9], v14 offset:1024
	ds_read_b128 v[10:13], v14 offset:2048
	ds_read_b128 v[14:17], v14 offset:3072
	ds_read_b128 v[18:21], v30
	ds_read_b128 v[22:25], v30 offset:1024
	ds_read_b128 v[26:29], v30 offset:2048
	ds_read_b128 v[30:33], v30 offset:3072
	s_add_u32 s26, s26, 0x20000
	s_addc_u32 s27, s27, 0
	s_mov_b32 m0, s34
	v_lshl_add_u64 v[226:227], s[26:27], 0, v[162:163]
	ds_read_b128 v[194:197], v190 offset:32768
	ds_read_b128 v[198:201], v190 offset:33792
	ds_read_b128 v[202:205], v190 offset:34816
	ds_read_b128 v[206:209], v190 offset:35840
	ds_read_b128 v[210:213], v190 offset:36864
	ds_read_b128 v[214:217], v190 offset:37888
	ds_read_b128 v[218:221], v190 offset:38912
	ds_read_b128 v[222:225], v190 offset:39936
	global_load_lds_dwordx4 v[226:227], off
	v_lshl_add_u64 v[226:227], s[26:27], 0, v[166:167]
	s_mov_b32 m0, s35
	s_nop 0
	global_load_lds_dwordx4 v[226:227], off
	s_waitcnt vmcnt(8)
	s_waitcnt lgkmcnt(0)
	s_barrier
	s_setprio 1
	s_nop 3
	s_waitcnt lgkmcnt(0)
	v_mfma_scale_f32_16x16x128_f8f6f4 v[158:161], v[2:9], v[194:201], v[158:161], v191, v192 op_sel_hi:[0,0,0]
	v_mfma_scale_f32_16x16x128_f8f6f4 v[154:157], v[10:17], v[194:201], v[154:157], v191, v192 op_sel_hi:[0,0,0]
	v_mfma_scale_f32_16x16x128_f8f6f4 v[142:145], v[2:9], v[202:209], v[142:145], v191, v192 op_sel_hi:[0,0,0]
	v_mfma_scale_f32_16x16x128_f8f6f4 v[138:141], v[10:17], v[202:209], v[138:141], v191, v192 op_sel_hi:[0,0,0]
	v_mfma_scale_f32_16x16x128_f8f6f4 v[126:129], v[2:9], v[210:217], v[126:129], v191, v192 op_sel_hi:[0,0,0]
	v_mfma_scale_f32_16x16x128_f8f6f4 v[122:125], v[10:17], v[210:217], v[122:125], v191, v192 op_sel_hi:[0,0,0]
	v_mfma_scale_f32_16x16x128_f8f6f4 v[110:113], v[2:9], v[218:225], v[110:113], v191, v192 op_sel_hi:[0,0,0]
	v_mfma_scale_f32_16x16x128_f8f6f4 v[106:109], v[10:17], v[218:225], v[106:109], v191, v192 op_sel_hi:[0,0,0]
	s_setprio 0
	s_setprio 1
	s_nop 3
	v_mfma_scale_f32_16x16x128_f8f6f4 v[150:153], v[18:25], v[194:201], v[150:153], v191, v192 op_sel_hi:[0,0,0]
	v_mfma_scale_f32_16x16x128_f8f6f4 v[146:149], v[26:33], v[194:201], v[146:149], v191, v192 op_sel_hi:[0,0,0]
	v_mfma_scale_f32_16x16x128_f8f6f4 v[134:137], v[18:25], v[202:209], v[134:137], v191, v192 op_sel_hi:[0,0,0]
	v_mfma_scale_f32_16x16x128_f8f6f4 v[130:133], v[26:33], v[202:209], v[130:133], v191, v192 op_sel_hi:[0,0,0]
	v_mfma_scale_f32_16x16x128_f8f6f4 v[118:121], v[18:25], v[210:217], v[118:121], v191, v192 op_sel_hi:[0,0,0]
	v_mfma_scale_f32_16x16x128_f8f6f4 v[114:117], v[26:33], v[210:217], v[114:117], v191, v192 op_sel_hi:[0,0,0]
	v_mfma_scale_f32_16x16x128_f8f6f4 v[102:105], v[18:25], v[218:225], v[102:105], v191, v192 op_sel_hi:[0,0,0]
	v_mfma_scale_f32_16x16x128_f8f6f4 v[98:101], v[26:33], v[218:225], v[98:101], v191, v192 op_sel_hi:[0,0,0]
	s_setprio 0
	s_barrier
	s_add_i32 s26, s44, s28
	v_lshl_add_u64 v[178:179], v[178:179], 0, s[8:9]
	s_mov_b32 m0, s26
	ds_read_b128 v[194:197], v190 offset:49152
	ds_read_b128 v[198:201], v190 offset:50176
	ds_read_b128 v[202:205], v190 offset:51200
	ds_read_b128 v[206:209], v190 offset:52224
	ds_read_b128 v[210:213], v190 offset:53248
	ds_read_b128 v[214:217], v190 offset:54272
	ds_read_b128 v[218:221], v190 offset:55296
	ds_read_b128 v[222:225], v190 offset:56320
	global_load_lds_dwordx4 v[178:179], off
	s_add_i32 m0, s26, 0x2000
	s_add_u32 s24, s24, 0x2080
	v_lshl_add_u64 v[178:179], v[180:181], 0, s[8:9]
	s_addc_u32 s25, s25, 0
	s_add_i32 s26, s45, s28
	global_load_lds_dwordx4 v[178:179], off
	v_lshl_add_u64 v[178:179], s[24:25], 0, v[164:165]
	s_mov_b32 m0, s26
	s_nop 0
	global_load_lds_dwordx4 v[178:179], off
	v_lshl_add_u64 v[178:179], s[24:25], 0, v[168:169]
	s_add_i32 m0, s26, 0x2000
	s_nop 0
	global_load_lds_dwordx4 v[178:179], off
	v_lshl_add_u64 v[178:179], v[182:183], 0, s[8:9]
	s_mov_b32 m0, s38
	s_nop 0
	global_load_lds_dwordx4 v[178:179], off
	v_lshl_add_u64 v[178:179], v[184:185], 0, s[8:9]
	s_mov_b32 m0, s39
	s_nop 0
	global_load_lds_dwordx4 v[178:179], off
	s_waitcnt vmcnt(8)
	s_waitcnt lgkmcnt(0)
	s_barrier
	s_setprio 1
	s_nop 3
	s_waitcnt lgkmcnt(0)
	v_mfma_scale_f32_16x16x128_f8f6f4 v[94:97], v[2:9], v[194:201], v[94:97], v191, v192 op_sel_hi:[0,0,0]
	v_mfma_scale_f32_16x16x128_f8f6f4 v[90:93], v[10:17], v[194:201], v[90:93], v191, v192 op_sel_hi:[0,0,0]
	v_mfma_scale_f32_16x16x128_f8f6f4 v[78:81], v[2:9], v[202:209], v[78:81], v191, v192 op_sel_hi:[0,0,0]
	v_mfma_scale_f32_16x16x128_f8f6f4 v[74:77], v[10:17], v[202:209], v[74:77], v191, v192 op_sel_hi:[0,0,0]
	v_mfma_scale_f32_16x16x128_f8f6f4 v[62:65], v[2:9], v[210:217], v[62:65], v191, v192 op_sel_hi:[0,0,0]
	v_mfma_scale_f32_16x16x128_f8f6f4 v[58:61], v[10:17], v[210:217], v[58:61], v191, v192 op_sel_hi:[0,0,0]
	v_mfma_scale_f32_16x16x128_f8f6f4 v[46:49], v[2:9], v[218:225], v[46:49], v191, v192 op_sel_hi:[0,0,0]
	v_mfma_scale_f32_16x16x128_f8f6f4 v[42:45], v[10:17], v[218:225], v[42:45], v191, v192 op_sel_hi:[0,0,0]
	s_setprio 0
	s_setprio 1
	s_nop 3
	v_mfma_scale_f32_16x16x128_f8f6f4 v[86:89], v[18:25], v[194:201], v[86:89], v191, v192 op_sel_hi:[0,0,0]
	v_mfma_scale_f32_16x16x128_f8f6f4 v[82:85], v[26:33], v[194:201], v[82:85], v191, v192 op_sel_hi:[0,0,0]
	v_mfma_scale_f32_16x16x128_f8f6f4 v[70:73], v[18:25], v[202:209], v[70:73], v191, v192 op_sel_hi:[0,0,0]
	v_mfma_scale_f32_16x16x128_f8f6f4 v[66:69], v[26:33], v[202:209], v[66:69], v191, v192 op_sel_hi:[0,0,0]
	v_mfma_scale_f32_16x16x128_f8f6f4 v[54:57], v[18:25], v[210:217], v[54:57], v191, v192 op_sel_hi:[0,0,0]
	v_mfma_scale_f32_16x16x128_f8f6f4 v[50:53], v[26:33], v[210:217], v[50:53], v191, v192 op_sel_hi:[0,0,0]
	v_mfma_scale_f32_16x16x128_f8f6f4 v[38:41], v[18:25], v[218:225], v[38:41], v191, v192 op_sel_hi:[0,0,0]
	v_mfma_scale_f32_16x16x128_f8f6f4 v[34:37], v[26:33], v[218:225], v[34:37], v191, v192 op_sel_hi:[0,0,0]
	s_setprio 0
	s_add_i32 s43, s43, 2
	s_add_u32 s22, s22, 0x100
	s_addc_u32 s23, s23, 0
	s_add_u32 s33, s33, 0x100
	s_addc_u32 s42, s42, 0
	s_cmp_gt_u32 s43, 5
	s_barrier
	s_cbranch_scc0 .LBB0_474
	s_and_b64 vcc, exec, s[10:11]
	s_cbranch_vccz .LBB0_477
	s_barrier

; #define PG8_STAGE(bufoff, gbase, voff) do { _Pragma("unroll") for (int _i = 0; _i < 2; ++_i) \
;         __builtin_amdgcn_global_load_lds((const unsigned*)((const char*)(gbase) + (voff)[_i]), (PG8_LAS unsigned*)(lds + (bufoff) + ldsw + _i * 8192), 16, 0, 0); } while (0)
; #define PG8_STAGE_A(bufoff, gbase, h, nx) do { if constexpr (Sched::GATHER) { const unsigned vv_[2] = {(nx) ? vAn[h][0] : vA[h][0], (nx) ? vAn[h][1] : vA[h][1]}; PG8_STAGE(bufoff, gbase, vv_); } \
;         else { PG8_STAGE(bufoff, (gbase) + (h) * hstep, voffA); } } while (0)
; #define PG8_LDA(dst, b, h) do { _Pragma("unroll") for (int m = 0; m < 4; ++m) _Pragma("unroll") for (int k = 0; k < 2; ++k) dst[m][k] = *(const PG8_LAS bf16x8*)(lds + PG8_SA(b, h) + aoff + m * 2048 + k * 1024); } while (0)
; #define PG8_LDB(dst, b, h) do { _Pragma("unroll") for (int n = 0; n < 2; ++n) _Pragma("unroll") for (int k = 0; k < 2; ++k) dst[n][k] = *(const PG8_LAS bf16x8*)(lds + PG8_SB(b, h) + boff + n * 2048 + k * 1024); } while (0)
; #define PG8_WAIT_V(n) asm volatile("s_waitcnt vmcnt(" #n ")" ::: "memory")
; #define PG8_WAIT_L(n) asm volatile("s_waitcnt lgkmcnt(" #n ")" ::: "memory")
; #define PG8_BAR __builtin_amdgcn_s_barrier()
; #define PG8_SCHED __builtin_amdgcn_sched_barrier(0)
;     ...
;             PG8_LDB(B0, 0, 0); PG8_LDB(B1, 0, 1); PG8_SCHED; PG8_LDA(At, 0, 0); PG8_STAGE_A(PG8_SA(1, 1), a1, 1, false);
;             PG8_WAIT_V(8); PG8_WAIT_L(0); PG8_BAR; PG8_MMA(0, 0, At, B0); PG8_MMA(0, 1, At, B1); PG8_BAR; PG8_SCHED;
;             PG8_LDA(At, 0, 1); PG8_STAGE(PG8_SB(0, 0), b2, voffB); PG8_STAGE(PG8_SB(0, 1), b2 + hstepB, voffB); PG8_STAGE_A(PG8_SA(0, 0), a2, 0, last);
;             PG8_WAIT_V(8); PG8_WAIT_L(0); PG8_BAR; PG8_MMA(1, 0, At, B0); PG8_MMA(1, 1, At, B1); PG8_BAR; PG8_SCHED;
.LBB0_841:
	ds_read_b128 v[26:29], v194
	ds_read_b128 v[30:33], v194 offset:1024
	ds_read_b128 v[18:21], v194 offset:2048
	ds_read_b128 v[22:25], v194 offset:3072
	ds_read_b128 v[10:13], v195
	ds_read_b128 v[14:17], v195 offset:1024
	ds_read_b128 v[2:5], v195 offset:2048
	ds_read_b128 v[6:9], v195 offset:3072
	s_add_u32 s20, s54, s4
	s_addc_u32 s21, s55, s5
	s_add_u32 s22, s20, 0x25400100
	s_addc_u32 s23, s21, 0
	s_add_u32 s52, s49, s4
	s_addc_u32 s53, s50, s5
	s_cmpk_eq_i32 s4, 0x300
	s_cselect_b64 vcc, -1, 0
	s_and_b64 s[20:21], vcc, exec
	s_cselect_b32 s23, s93, s23
	s_cselect_b32 s22, s92, s22
	s_cselect_b32 s21, s17, s53
	s_cselect_b32 s20, s48, s52
	s_mov_b32 m0, s36
	v_lshl_add_u64 v[232:233], v[180:181], 0, s[4:5]
	ds_read_b128 v[182:185], v196
	ds_read_b128 v[186:189], v196 offset:1024
	ds_read_b128 v[208:211], v196 offset:2048
	ds_read_b128 v[212:215], v196 offset:3072
	ds_read_b128 v[216:219], v196 offset:4096
	ds_read_b128 v[220:223], v196 offset:5120
	ds_read_b128 v[224:227], v196 offset:6144
	ds_read_b128 v[228:231], v196 offset:7168
	global_load_lds_dwordx4 v[232:233], off
	v_lshl_add_u64 v[232:233], v[178:179], 0, s[4:5]
	s_mov_b32 m0, s37
	s_nop 0
	global_load_lds_dwordx4 v[232:233], off
	s_waitcnt vmcnt(8)
	s_waitcnt lgkmcnt(0)
	s_barrier
	s_setprio 1
	s_nop 3
	s_waitcnt lgkmcnt(0)
	v_mfma_scale_f32_16x16x128_f8f6f4 v[158:161], v[26:33], v[182:189], v[158:161], v197, v198 op_sel_hi:[0,0,0]
	v_mfma_scale_f32_16x16x128_f8f6f4 v[150:153], v[18:25], v[182:189], v[150:153], v197, v198 op_sel_hi:[0,0,0]
	v_mfma_scale_f32_16x16x128_f8f6f4 v[142:145], v[26:33], v[208:215], v[142:145], v197, v198 op_sel_hi:[0,0,0]
	v_mfma_scale_f32_16x16x128_f8f6f4 v[134:137], v[18:25], v[208:215], v[134:137], v197, v198 op_sel_hi:[0,0,0]
	v_mfma_scale_f32_16x16x128_f8f6f4 v[126:129], v[26:33], v[216:223], v[126:129], v197, v198 op_sel_hi:[0,0,0]
	v_mfma_scale_f32_16x16x128_f8f6f4 v[118:121], v[18:25], v[216:223], v[118:121], v197, v198 op_sel_hi:[0,0,0]
	v_mfma_scale_f32_16x16x128_f8f6f4 v[110:113], v[26:33], v[224:231], v[110:113], v197, v198 op_sel_hi:[0,0,0]
	v_mfma_scale_f32_16x16x128_f8f6f4 v[98:101], v[18:25], v[224:231], v[98:101], v197, v198 op_sel_hi:[0,0,0]
	s_setprio 0
	s_setprio 1
	s_nop 3
	v_mfma_scale_f32_16x16x128_f8f6f4 v[154:157], v[10:17], v[182:189], v[154:157], v197, v198 op_sel_hi:[0,0,0]
	v_mfma_scale_f32_16x16x128_f8f6f4 v[146:149], v[2:9], v[182:189], v[146:149], v197, v198 op_sel_hi:[0,0,0]
	v_mfma_scale_f32_16x16x128_f8f6f4 v[138:141], v[10:17], v[208:215], v[138:141], v197, v198 op_sel_hi:[0,0,0]
	v_mfma_scale_f32_16x16x128_f8f6f4 v[130:133], v[2:9], v[208:215], v[130:133], v197, v198 op_sel_hi:[0,0,0]
	v_mfma_scale_f32_16x16x128_f8f6f4 v[122:125], v[10:17], v[216:223], v[122:125], v197, v198 op_sel_hi:[0,0,0]
	v_mfma_scale_f32_16x16x128_f8f6f4 v[114:117], v[2:9], v[216:223], v[114:117], v197, v198 op_sel_hi:[0,0,0]
	v_mfma_scale_f32_16x16x128_f8f6f4 v[106:109], v[10:17], v[224:231], v[106:109], v197, v198 op_sel_hi:[0,0,0]
	v_mfma_scale_f32_16x16x128_f8f6f4 v[94:97], v[2:9], v[224:231], v[94:97], v197, v198 op_sel_hi:[0,0,0]
	s_setprio 0
	s_barrier
	s_mov_b32 m0, s38
	v_lshl_add_u64 v[182:183], s[20:21], 0, v[164:165]
	s_add_u32 s52, s20, 0x20000
	ds_read_b128 v[208:211], v196 offset:16384
	ds_read_b128 v[212:215], v196 offset:17408
	ds_read_b128 v[216:219], v196 offset:18432
	ds_read_b128 v[220:223], v196 offset:19456
	ds_read_b128 v[224:227], v196 offset:20480
	ds_read_b128 v[228:231], v196 offset:21504
	ds_read_b128 v[232:235], v196 offset:22528
	ds_read_b128 v[236:239], v196 offset:23552
	global_load_lds_dwordx4 v[182:183], off
	v_lshl_add_u64 v[184:185], s[20:21], 0, v[162:163]
	s_mov_b32 m0, s39
	s_addc_u32 s53, s21, 0
	global_load_lds_dwordx4 v[184:185], off
	v_lshl_add_u64 v[186:187], s[52:53], 0, v[164:165]
	s_mov_b32 m0, s40
	v_cndmask_b32_e32 v166, v206, v202, vcc
	global_load_lds_dwordx4 v[186:187], off
	v_lshl_add_u64 v[186:187], s[52:53], 0, v[162:163]
	s_mov_b32 m0, s41
	v_lshl_add_u64 v[188:189], s[22:23], 0, v[166:167]
	global_load_lds_dwordx4 v[186:187], off
	s_mov_b32 m0, s26
	v_cndmask_b32_e32 v186, v172, v203, vcc
	global_load_lds_dwordx4 v166, s[22:23]
	s_mov_b32 m0, s27
	v_mov_b32_e32 v187, v167
	global_load_lds_dwordx4 v186, s[22:23]
	s_waitcnt vmcnt(8)
	s_waitcnt lgkmcnt(0)
	v_lshl_add_u64 v[186:187], s[22:23], 0, v[186:187]
	s_barrier
	s_setprio 1
	s_nop 3
	s_waitcnt lgkmcnt(0)
	v_mfma_scale_f32_16x16x128_f8f6f4 v[82:85], v[26:33], v[208:215], v[82:85], v197, v198 op_sel_hi:[0,0,0]
	v_mfma_scale_f32_16x16x128_f8f6f4 v[70:73], v[18:25], v[208:215], v[70:73], v197, v198 op_sel_hi:[0,0,0]
	v_mfma_scale_f32_16x16x128_f8f6f4 v[78:81], v[26:33], v[216:223], v[78:81], v197, v198 op_sel_hi:[0,0,0]
	v_mfma_scale_f32_16x16x128_f8f6f4 v[66:69], v[18:25], v[216:223], v[66:69], v197, v198 op_sel_hi:[0,0,0]
	v_mfma_scale_f32_16x16x128_f8f6f4 v[58:61], v[26:33], v[224:231], v[58:61], v197, v198 op_sel_hi:[0,0,0]
	v_mfma_scale_f32_16x16x128_f8f6f4 v[50:53], v[18:25], v[224:231], v[50:53], v197, v198 op_sel_hi:[0,0,0]
	v_mfma_scale_f32_16x16x128_f8f6f4 v[42:45], v[26:33], v[232:239], v[42:45], v197, v198 op_sel_hi:[0,0,0]
	v_mfma_scale_f32_16x16x128_f8f6f4 v[34:37], v[18:25], v[232:239], v[34:37], v197, v198 op_sel_hi:[0,0,0]
	s_setprio 0
	s_setprio 1
	s_nop 3
	v_mfma_scale_f32_16x16x128_f8f6f4 v[102:105], v[10:17], v[208:215], v[102:105], v197, v198 op_sel_hi:[0,0,0]
	v_mfma_scale_f32_16x16x128_f8f6f4 v[90:93], v[2:9], v[208:215], v[90:93], v197, v198 op_sel_hi:[0,0,0]
	v_mfma_scale_f32_16x16x128_f8f6f4 v[86:89], v[10:17], v[216:223], v[86:89], v197, v198 op_sel_hi:[0,0,0]
	v_mfma_scale_f32_16x16x128_f8f6f4 v[74:77], v[2:9], v[216:223], v[74:77], v197, v198 op_sel_hi:[0,0,0]
	v_mfma_scale_f32_16x16x128_f8f6f4 v[62:65], v[10:17], v[224:231], v[62:65], v197, v198 op_sel_hi:[0,0,0]
	v_mfma_scale_f32_16x16x128_f8f6f4 v[54:57], v[2:9], v[224:231], v[54:57], v197, v198 op_sel_hi:[0,0,0]
	v_mfma_scale_f32_16x16x128_f8f6f4 v[46:49], v[10:17], v[232:239], v[46:49], v197, v198 op_sel_hi:[0,0,0]
	v_mfma_scale_f32_16x16x128_f8f6f4 v[38:41], v[2:9], v[232:239], v[38:41], v197, v198 op_sel_hi:[0,0,0]
	s_setprio 0
	s_barrier
; #define PG8_STAGE(bufoff, gbase, voff) do { _Pragma("unroll") for (int _i = 0; _i < 2; ++_i) \
;         __builtin_amdgcn_global_load_lds((const unsigned*)((const char*)(gbase) + (voff)[_i]), (PG8_LAS unsigned*)(lds + (bufoff) + ldsw + _i * 8192), 16, 0, 0); } while (0)
; #define PG8_STAGE_A(bufoff, gbase, h, nx) do { if constexpr (Sched::GATHER) { const unsigned vv_[2] = {(nx) ? vAn[h][0] : vA[h][0], (nx) ? vAn[h][1] : vA[h][1]}; PG8_STAGE(bufoff, gbase, vv_); } \
;         else { PG8_STAGE(bufoff, (gbase) + (h) * hstep, voffA); } } while (0)
; #define PG8_LDA(dst, b, h) do { _Pragma("unroll") for (int m = 0; m < 4; ++m) _Pragma("unroll") for (int k = 0; k < 2; ++k) dst[m][k] = *(const PG8_LAS bf16x8*)(lds + PG8_SA(b, h) + aoff + m * 2048 + k * 1024); } while (0)
; #define PG8_LDB(dst, b, h) do { _Pragma("unroll") for (int n = 0; n < 2; ++n) _Pragma("unroll") for (int k = 0; k < 2; ++k) dst[n][k] = *(const PG8_LAS bf16x8*)(lds + PG8_SB(b, h) + boff + n * 2048 + k * 1024); } while (0)
; #define PG8_WAIT_V(n) asm volatile("s_waitcnt vmcnt(" #n ")" ::: "memory")
; #define PG8_WAIT_L(n) asm volatile("s_waitcnt lgkmcnt(" #n ")" ::: "memory")
; #define PG8_BAR __builtin_amdgcn_s_barrier()
; #define PG8_SCHED __builtin_amdgcn_sched_barrier(0)
;     ...
;         for (int t = 0; t < nt; t += 2) {
;     ...
;             PG8_LDB(B0, 1, 0); PG8_LDB(B1, 1, 1); PG8_SCHED; PG8_LDA(At, 1, 0); PG8_STAGE_A(PG8_SA(0, 1), a2, 1, last);
;             PG8_WAIT_V(8); PG8_WAIT_L(0); PG8_BAR; PG8_MMA(0, 0, At, B0); PG8_MMA(0, 1, At, B1); PG8_BAR; PG8_SCHED;
;             PG8_LDA(At, 1, 1); PG8_STAGE(PG8_SB(1, 0), b3, voffB); PG8_STAGE(PG8_SB(1, 1), b3 + hstepB, voffB); PG8_STAGE_A(PG8_SA(1, 0), a3, 0, last);
;             PG8_WAIT_V(8); PG8_WAIT_L(0); PG8_BAR; PG8_MMA(1, 0, At, B0); PG8_MMA(1, 1, At, B1); PG8_BAR; PG8_SCHED;
	ds_read_b128 v[2:5], v199
	ds_read_b128 v[6:9], v199 offset:1024
	ds_read_b128 v[10:13], v199 offset:2048
	ds_read_b128 v[14:17], v199 offset:3072
	ds_read_b128 v[18:21], v200
	ds_read_b128 v[22:25], v200 offset:1024
	ds_read_b128 v[26:29], v200 offset:2048
	ds_read_b128 v[30:33], v200 offset:3072
	s_mov_b32 m0, s28
	v_cndmask_b32_e32 v166, v174, v204, vcc
	ds_read_b128 v[208:211], v196 offset:32768
	ds_read_b128 v[212:215], v196 offset:33792
	ds_read_b128 v[216:219], v196 offset:34816
	ds_read_b128 v[220:223], v196 offset:35840
	ds_read_b128 v[224:227], v196 offset:36864
	ds_read_b128 v[228:231], v196 offset:37888
	ds_read_b128 v[232:235], v196 offset:38912
	ds_read_b128 v[236:239], v196 offset:39936
	v_cndmask_b32_e32 v175, v176, v205, vcc
	global_load_lds_dwordx4 v166, s[22:23]
	s_mov_b32 m0, s29
	s_nop 0
	global_load_lds_dwordx4 v175, s[22:23]
	s_waitcnt vmcnt(8)
	s_waitcnt lgkmcnt(0)
	s_barrier
	s_setprio 1
	s_nop 3
	s_waitcnt lgkmcnt(0)
	v_mfma_scale_f32_16x16x128_f8f6f4 v[158:161], v[2:9], v[208:215], v[158:161], v197, v198 op_sel_hi:[0,0,0]
	v_mfma_scale_f32_16x16x128_f8f6f4 v[150:153], v[10:17], v[208:215], v[150:153], v197, v198 op_sel_hi:[0,0,0]
	v_mfma_scale_f32_16x16x128_f8f6f4 v[142:145], v[2:9], v[216:223], v[142:145], v197, v198 op_sel_hi:[0,0,0]
	v_mfma_scale_f32_16x16x128_f8f6f4 v[134:137], v[10:17], v[216:223], v[134:137], v197, v198 op_sel_hi:[0,0,0]
	v_mfma_scale_f32_16x16x128_f8f6f4 v[126:129], v[2:9], v[224:231], v[126:129], v197, v198 op_sel_hi:[0,0,0]
	v_mfma_scale_f32_16x16x128_f8f6f4 v[118:121], v[10:17], v[224:231], v[118:121], v197, v198 op_sel_hi:[0,0,0]
	v_mfma_scale_f32_16x16x128_f8f6f4 v[110:113], v[2:9], v[232:239], v[110:113], v197, v198 op_sel_hi:[0,0,0]
	v_mfma_scale_f32_16x16x128_f8f6f4 v[98:101], v[10:17], v[232:239], v[98:101], v197, v198 op_sel_hi:[0,0,0]
	s_setprio 0
	s_setprio 1
	s_nop 3
	v_mfma_scale_f32_16x16x128_f8f6f4 v[154:157], v[18:25], v[208:215], v[154:157], v197, v198 op_sel_hi:[0,0,0]
	v_mfma_scale_f32_16x16x128_f8f6f4 v[146:149], v[26:33], v[208:215], v[146:149], v197, v198 op_sel_hi:[0,0,0]
	v_mfma_scale_f32_16x16x128_f8f6f4 v[138:141], v[18:25], v[216:223], v[138:141], v197, v198 op_sel_hi:[0,0,0]
	v_mfma_scale_f32_16x16x128_f8f6f4 v[130:133], v[26:33], v[216:223], v[130:133], v197, v198 op_sel_hi:[0,0,0]
	v_mfma_scale_f32_16x16x128_f8f6f4 v[122:125], v[18:25], v[224:231], v[122:125], v197, v198 op_sel_hi:[0,0,0]
	v_mfma_scale_f32_16x16x128_f8f6f4 v[114:117], v[26:33], v[224:231], v[114:117], v197, v198 op_sel_hi:[0,0,0]
	v_mfma_scale_f32_16x16x128_f8f6f4 v[106:109], v[18:25], v[232:239], v[106:109], v197, v198 op_sel_hi:[0,0,0]
	v_mfma_scale_f32_16x16x128_f8f6f4 v[94:97], v[26:33], v[232:239], v[94:97], v197, v198 op_sel_hi:[0,0,0]
	s_setprio 0
	s_barrier
	s_mov_b32 m0, s42
	v_lshl_add_u64 v[182:183], v[182:183], 0, s[10:11]
	s_add_u32 s20, s20, 0x20080
	ds_read_b128 v[208:211], v196 offset:49152
	ds_read_b128 v[212:215], v196 offset:50176
	ds_read_b128 v[216:219], v196 offset:51200
	ds_read_b128 v[220:223], v196 offset:52224
	ds_read_b128 v[224:227], v196 offset:53248
	ds_read_b128 v[228:231], v196 offset:54272
	ds_read_b128 v[232:235], v196 offset:55296
	ds_read_b128 v[236:239], v196 offset:56320
	global_load_lds_dwordx4 v[182:183], off
	v_lshl_add_u64 v[182:183], v[184:185], 0, s[10:11]
	s_mov_b32 m0, s43
	s_addc_u32 s21, s21, 0
	global_load_lds_dwordx4 v[182:183], off
	v_lshl_add_u64 v[182:183], s[20:21], 0, v[164:165]
	s_mov_b32 m0, s44
	s_nop 0
	global_load_lds_dwordx4 v[182:183], off
	v_lshl_add_u64 v[182:183], s[20:21], 0, v[162:163]
	s_add_i32 m0, s44, 0x2000
	s_nop 0
	global_load_lds_dwordx4 v[182:183], off
	v_lshl_add_u64 v[182:183], v[188:189], 0, s[10:11]
	s_mov_b32 m0, s31
	s_nop 0
	global_load_lds_dwordx4 v[182:183], off
	v_lshl_add_u64 v[182:183], v[186:187], 0, s[10:11]
	s_mov_b32 m0, s34
	s_nop 0
	global_load_lds_dwordx4 v[182:183], off
	s_waitcnt vmcnt(8)
	s_waitcnt lgkmcnt(0)
	s_barrier
	s_setprio 1
	s_nop 3
	s_waitcnt lgkmcnt(0)
	v_mfma_scale_f32_16x16x128_f8f6f4 v[82:85], v[2:9], v[208:215], v[82:85], v197, v198 op_sel_hi:[0,0,0]
	v_mfma_scale_f32_16x16x128_f8f6f4 v[70:73], v[10:17], v[208:215], v[70:73], v197, v198 op_sel_hi:[0,0,0]
	v_mfma_scale_f32_16x16x128_f8f6f4 v[78:81], v[2:9], v[216:223], v[78:81], v197, v198 op_sel_hi:[0,0,0]
	v_mfma_scale_f32_16x16x128_f8f6f4 v[66:69], v[10:17], v[216:223], v[66:69], v197, v198 op_sel_hi:[0,0,0]
	v_mfma_scale_f32_16x16x128_f8f6f4 v[58:61], v[2:9], v[224:231], v[58:61], v197, v198 op_sel_hi:[0,0,0]
	v_mfma_scale_f32_16x16x128_f8f6f4 v[50:53], v[10:17], v[224:231], v[50:53], v197, v198 op_sel_hi:[0,0,0]
	v_mfma_scale_f32_16x16x128_f8f6f4 v[42:45], v[2:9], v[232:239], v[42:45], v197, v198 op_sel_hi:[0,0,0]
	v_mfma_scale_f32_16x16x128_f8f6f4 v[34:37], v[10:17], v[232:239], v[34:37], v197, v198 op_sel_hi:[0,0,0]
	s_setprio 0
	s_setprio 1
	s_nop 3
	v_mfma_scale_f32_16x16x128_f8f6f4 v[102:105], v[18:25], v[208:215], v[102:105], v197, v198 op_sel_hi:[0,0,0]
	v_mfma_scale_f32_16x16x128_f8f6f4 v[90:93], v[26:33], v[208:215], v[90:93], v197, v198 op_sel_hi:[0,0,0]
	v_mfma_scale_f32_16x16x128_f8f6f4 v[86:89], v[18:25], v[216:223], v[86:89], v197, v198 op_sel_hi:[0,0,0]
	v_mfma_scale_f32_16x16x128_f8f6f4 v[74:77], v[26:33], v[216:223], v[74:77], v197, v198 op_sel_hi:[0,0,0]
	v_mfma_scale_f32_16x16x128_f8f6f4 v[62:65], v[18:25], v[224:231], v[62:65], v197, v198 op_sel_hi:[0,0,0]
	v_mfma_scale_f32_16x16x128_f8f6f4 v[54:57], v[26:33], v[224:231], v[54:57], v197, v198 op_sel_hi:[0,0,0]
	v_mfma_scale_f32_16x16x128_f8f6f4 v[46:49], v[18:25], v[232:239], v[46:49], v197, v198 op_sel_hi:[0,0,0]
	v_mfma_scale_f32_16x16x128_f8f6f4 v[38:41], v[26:33], v[232:239], v[38:41], v197, v198 op_sel_hi:[0,0,0]
	s_setprio 0
	s_add_i32 s51, s51, 2
	s_add_u32 s4, s4, 0x100
	s_addc_u32 s5, s5, 0
	s_cmp_gt_u32 s51, 5
	s_barrier
	s_cbranch_scc0 .LBB0_841
	s_and_b64 vcc, exec, s[14:15]
	s_cbranch_vccz .LBB0_844
	s_barrier

; #define PG8_STAGE(bufoff, gbase, voff) do { _Pragma("unroll") for (int _i = 0; _i < 2; ++_i) \
;         __builtin_amdgcn_global_load_lds((const unsigned*)((const char*)(gbase) + (voff)[_i]), (PG8_LAS unsigned*)(lds + (bufoff) + ldsw + _i * 8192), 16, 0, 0); } while (0)
; #define PG8_STAGE_A(bufoff, gbase, h, nx) do { if constexpr (Sched::GATHER) { const unsigned vv_[2] = {(nx) ? vAn[h][0] : vA[h][0], (nx) ? vAn[h][1] : vA[h][1]}; PG8_STAGE(bufoff, gbase, vv_); } \
;         else { PG8_STAGE(bufoff, (gbase) + (h) * hstep, voffA); } } while (0)
; #define PG8_LDA(dst, b, h) do { _Pragma("unroll") for (int m = 0; m < 4; ++m) _Pragma("unroll") for (int k = 0; k < 2; ++k) dst[m][k] = *(const PG8_LAS bf16x8*)(lds + PG8_SA(b, h) + aoff + m * 2048 + k * 1024); } while (0)
; #define PG8_WAIT_V(n) asm volatile("s_waitcnt vmcnt(" #n ")" ::: "memory")
; #define PG8_WAIT_L(n) asm volatile("s_waitcnt lgkmcnt(" #n ")" ::: "memory")
; #define PG8_BAR __builtin_amdgcn_s_barrier()
; #define PG8_SCHED __builtin_amdgcn_sched_barrier(0)
;     ...
;         for (int t = 0; t < nt; t += 2) {
;     ...
;             PG8_WAIT_V(8); PG8_WAIT_L(0); PG8_BAR; PG8_MMA(0, 0, At, B0); PG8_MMA(0, 1, At, B1); PG8_BAR; PG8_SCHED;
;             PG8_LDA(At, 1, 1); PG8_STAGE(PG8_SB(1, 0), b3, voffB); PG8_STAGE(PG8_SB(1, 1), b3 + hstepB, voffB); PG8_STAGE_A(PG8_SA(1, 0), a3, 0, last);
;             PG8_WAIT_V(8); PG8_WAIT_L(0); PG8_BAR; PG8_MMA(1, 0, At, B0); PG8_MMA(1, 1, At, B1); PG8_BAR; PG8_SCHED;
.Lgate9_skip:
	s_waitcnt lgkmcnt(0)
	s_barrier
	s_setprio 1
	s_nop 3
	s_waitcnt lgkmcnt(0)
	v_mfma_scale_f32_16x16x128_f8f6f4 v[94:97], v[2:9], v[194:201], v[94:97], v191, v192 op_sel_hi:[0,0,0]
	v_mfma_scale_f32_16x16x128_f8f6f4 v[90:93], v[10:17], v[194:201], v[90:93], v191, v192 op_sel_hi:[0,0,0]
	v_mfma_scale_f32_16x16x128_f8f6f4 v[78:81], v[2:9], v[202:209], v[78:81], v191, v192 op_sel_hi:[0,0,0]
	v_mfma_scale_f32_16x16x128_f8f6f4 v[74:77], v[10:17], v[202:209], v[74:77], v191, v192 op_sel_hi:[0,0,0]
	v_mfma_scale_f32_16x16x128_f8f6f4 v[62:65], v[2:9], v[210:217], v[62:65], v191, v192 op_sel_hi:[0,0,0]
	v_mfma_scale_f32_16x16x128_f8f6f4 v[58:61], v[10:17], v[210:217], v[58:61], v191, v192 op_sel_hi:[0,0,0]
	v_mfma_scale_f32_16x16x128_f8f6f4 v[46:49], v[2:9], v[218:225], v[46:49], v191, v192 op_sel_hi:[0,0,0]
	v_mfma_scale_f32_16x16x128_f8f6f4 v[42:45], v[10:17], v[218:225], v[42:45], v191, v192 op_sel_hi:[0,0,0]
	s_setprio 0
	s_setprio 1
	s_nop 3
	v_mfma_scale_f32_16x16x128_f8f6f4 v[86:89], v[18:25], v[194:201], v[86:89], v191, v192 op_sel_hi:[0,0,0]
	v_mfma_scale_f32_16x16x128_f8f6f4 v[82:85], v[26:33], v[194:201], v[82:85], v191, v192 op_sel_hi:[0,0,0]
	v_mfma_scale_f32_16x16x128_f8f6f4 v[70:73], v[18:25], v[202:209], v[70:73], v191, v192 op_sel_hi:[0,0,0]
	v_mfma_scale_f32_16x16x128_f8f6f4 v[66:69], v[26:33], v[202:209], v[66:69], v191, v192 op_sel_hi:[0,0,0]
	v_mfma_scale_f32_16x16x128_f8f6f4 v[54:57], v[18:25], v[210:217], v[54:57], v191, v192 op_sel_hi:[0,0,0]
	v_mfma_scale_f32_16x16x128_f8f6f4 v[50:53], v[26:33], v[210:217], v[50:53], v191, v192 op_sel_hi:[0,0,0]
	v_mfma_scale_f32_16x16x128_f8f6f4 v[38:41], v[18:25], v[218:225], v[38:41], v191, v192 op_sel_hi:[0,0,0]
	v_mfma_scale_f32_16x16x128_f8f6f4 v[34:37], v[26:33], v[218:225], v[34:37], v191, v192 op_sel_hi:[0,0,0]
	s_setprio 0
	s_add_i32 s47, s47, 2
	s_add_u32 s22, s22, 0x100
	s_addc_u32 s23, s23, 0
	s_add_u32 s45, s45, 0x100
	s_addc_u32 s46, s46, 0
	s_cmp_gt_u32 s47, 13
	s_barrier
	s_cbranch_scc0 .LBB0_895
	s_and_b64 vcc, exec, s[10:11]
	s_cbranch_vccz .LBB0_898
	s_barrier

; #define PG8_STAGE(bufoff, gbase, voff) do { _Pragma("unroll") for (int _i = 0; _i < 2; ++_i) \
;         __builtin_amdgcn_global_load_lds((const unsigned*)((const char*)(gbase) + (voff)[_i]), (PG8_LAS unsigned*)(lds + (bufoff) + ldsw + _i * 8192), 16, 0, 0); } while (0)
; #define PG8_STAGE_A(bufoff, gbase, h, nx) do { if constexpr (Sched::GATHER) { const unsigned vv_[2] = {(nx) ? vAn[h][0] : vA[h][0], (nx) ? vAn[h][1] : vA[h][1]}; PG8_STAGE(bufoff, gbase, vv_); } \
;         else { PG8_STAGE(bufoff, (gbase) + (h) * hstep, voffA); } } while (0)
; #define PG8_LDA(dst, b, h) do { _Pragma("unroll") for (int m = 0; m < 4; ++m) _Pragma("unroll") for (int k = 0; k < 2; ++k) dst[m][k] = *(const PG8_LAS bf16x8*)(lds + PG8_SA(b, h) + aoff + m * 2048 + k * 1024); } while (0)
; #define PG8_LDB(dst, b, h) do { _Pragma("unroll") for (int n = 0; n < 2; ++n) _Pragma("unroll") for (int k = 0; k < 2; ++k) dst[n][k] = *(const PG8_LAS bf16x8*)(lds + PG8_SB(b, h) + boff + n * 2048 + k * 1024); } while (0)
; #define PG8_WAIT_V(n) asm volatile("s_waitcnt vmcnt(" #n ")" ::: "memory")
; #define PG8_WAIT_L(n) asm volatile("s_waitcnt lgkmcnt(" #n ")" ::: "memory")
; #define PG8_BAR __builtin_amdgcn_s_barrier()
; #define PG8_SCHED __builtin_amdgcn_sched_barrier(0)
;     ...
;         for (int t = 0; t < nt; t += 2) {
;             const bool last = (t == nt - 2);
;             const char* a1 = cA + (size_t)(t + 1) * kstep;
;             const char* a2 = last ? nA : cA + (size_t)(t + 2) * kstep; const char* b2 = last ? nB : cB + (size_t)(t + 2) * kstep;
;             const char* a3 = a2 + kstep; const char* b3 = b2 + kstep;
;             if (last && has_next) S.a_ready(nxt);
;             if constexpr (SP2) {
;             PG8_LDB(B0, 0, 0); PG8_LDB(B1, 0, 1); PG8_SCHED; PG8_LDA(At, 0, 0); PG8_STAGE_A(PG8_SA(1, 1), a1, 1, false);
;             PG8_WAIT_V(8); PG8_WAIT_L(0); PG8_BAR; PG8_MMA(0, 0, At, B0); PG8_MMA(0, 1, At, B1); PG8_BAR; PG8_SCHED;
;             PG8_LDA(At, 0, 1); PG8_STAGE(PG8_SB(0, 0), b2, voffB); PG8_STAGE(PG8_SB(0, 1), b2 + hstepB, voffB); PG8_STAGE_A(PG8_SA(0, 0), a2, 0, last);
;             PG8_WAIT_V(8); PG8_WAIT_L(0); PG8_BAR; PG8_MMA(1, 0, At, B0); PG8_MMA(1, 1, At, B1); PG8_BAR; PG8_SCHED;
.LBB0_1026:
	ds_read_b128 v[26:29], v188
	ds_read_b128 v[30:33], v188 offset:1024
	ds_read_b128 v[18:21], v188 offset:2048
	ds_read_b128 v[22:25], v188 offset:3072
	ds_read_b128 v[10:13], v189
	ds_read_b128 v[14:17], v189 offset:1024
	ds_read_b128 v[2:5], v189 offset:2048
	ds_read_b128 v[6:9], v189 offset:3072
	s_add_u32 s52, s6, 0xfffe0080
	s_addc_u32 s53, s7, -1
	s_cmp_eq_u32 s73, 4
	s_cselect_b32 s55, s5, s53
	s_cselect_b32 s54, s33, s52
	s_cselect_b32 s53, s43, s72
	s_cselect_b32 s52, s45, s71
	v_lshl_add_u64 v[220:221], s[6:7], 0, v[170:171]
	s_add_i32 m0, s51, 0xc000
	ds_read_b128 v[178:181], v190
	ds_read_b128 v[182:185], v190 offset:1024
	ds_read_b128 v[196:199], v190 offset:2048
	ds_read_b128 v[200:203], v190 offset:3072
	ds_read_b128 v[204:207], v190 offset:4096
	ds_read_b128 v[208:211], v190 offset:5120
	ds_read_b128 v[212:215], v190 offset:6144
	ds_read_b128 v[216:219], v190 offset:7168
	global_load_lds_dwordx4 v[220:221], off
	v_lshl_add_u64 v[220:221], s[6:7], 0, v[172:173]
	s_add_i32 m0, s51, 0xe000
	s_nop 0
	global_load_lds_dwordx4 v[220:221], off
	s_waitcnt vmcnt(8)
	s_waitcnt lgkmcnt(0)
	s_barrier
	s_setprio 1
	s_nop 3
	s_waitcnt lgkmcnt(0)
	v_mfma_scale_f32_16x16x128_f8f6f4 v[158:161], v[26:33], v[178:185], v[158:161], v191, v192 op_sel_hi:[0,0,0]
	v_mfma_scale_f32_16x16x128_f8f6f4 v[154:157], v[18:25], v[178:185], v[154:157], v191, v192 op_sel_hi:[0,0,0]
	v_mfma_scale_f32_16x16x128_f8f6f4 v[142:145], v[26:33], v[196:203], v[142:145], v191, v192 op_sel_hi:[0,0,0]
	v_mfma_scale_f32_16x16x128_f8f6f4 v[138:141], v[18:25], v[196:203], v[138:141], v191, v192 op_sel_hi:[0,0,0]
	v_mfma_scale_f32_16x16x128_f8f6f4 v[126:129], v[26:33], v[204:211], v[126:129], v191, v192 op_sel_hi:[0,0,0]
	v_mfma_scale_f32_16x16x128_f8f6f4 v[122:125], v[18:25], v[204:211], v[122:125], v191, v192 op_sel_hi:[0,0,0]
	v_mfma_scale_f32_16x16x128_f8f6f4 v[110:113], v[26:33], v[212:219], v[110:113], v191, v192 op_sel_hi:[0,0,0]
	v_mfma_scale_f32_16x16x128_f8f6f4 v[106:109], v[18:25], v[212:219], v[106:109], v191, v192 op_sel_hi:[0,0,0]
	s_setprio 0
	s_setprio 1
	s_nop 3
	v_mfma_scale_f32_16x16x128_f8f6f4 v[150:153], v[10:17], v[178:185], v[150:153], v191, v192 op_sel_hi:[0,0,0]
	v_mfma_scale_f32_16x16x128_f8f6f4 v[146:149], v[2:9], v[178:185], v[146:149], v191, v192 op_sel_hi:[0,0,0]
	v_mfma_scale_f32_16x16x128_f8f6f4 v[134:137], v[10:17], v[196:203], v[134:137], v191, v192 op_sel_hi:[0,0,0]
	v_mfma_scale_f32_16x16x128_f8f6f4 v[130:133], v[2:9], v[196:203], v[130:133], v191, v192 op_sel_hi:[0,0,0]
	v_mfma_scale_f32_16x16x128_f8f6f4 v[118:121], v[10:17], v[204:211], v[118:121], v191, v192 op_sel_hi:[0,0,0]
	v_mfma_scale_f32_16x16x128_f8f6f4 v[114:117], v[2:9], v[204:211], v[114:117], v191, v192 op_sel_hi:[0,0,0]
	v_mfma_scale_f32_16x16x128_f8f6f4 v[102:105], v[10:17], v[212:219], v[102:105], v191, v192 op_sel_hi:[0,0,0]
	v_mfma_scale_f32_16x16x128_f8f6f4 v[98:101], v[2:9], v[212:219], v[98:101], v191, v192 op_sel_hi:[0,0,0]
	s_setprio 0
	s_barrier
	s_add_i32 s74, s67, s56
	v_lshl_add_u64 v[178:179], s[52:53], 0, v[164:165]
	s_mov_b32 m0, s74
	ds_read_b128 v[196:199], v190 offset:16384
	ds_read_b128 v[200:203], v190 offset:17408
	ds_read_b128 v[204:207], v190 offset:18432
	ds_read_b128 v[208:211], v190 offset:19456
	ds_read_b128 v[212:215], v190 offset:20480
	ds_read_b128 v[216:219], v190 offset:21504
	ds_read_b128 v[220:223], v190 offset:22528
	ds_read_b128 v[224:227], v190 offset:23552
	global_load_lds_dwordx4 v[178:179], off
	s_add_i32 m0, s74, 0x2000
	s_add_u32 s74, s52, 0x8000
	v_lshl_add_u64 v[180:181], s[52:53], 0, v[168:169]
	s_addc_u32 s75, s53, 0
	s_add_i32 s76, s68, s56
	global_load_lds_dwordx4 v[180:181], off
	v_lshl_add_u64 v[182:183], s[74:75], 0, v[164:165]
	s_mov_b32 m0, s76
	v_lshl_add_u64 v[184:185], s[54:55], 0, v[166:167]
	global_load_lds_dwordx4 v[182:183], off
	v_lshl_add_u64 v[182:183], s[74:75], 0, v[168:169]
	s_add_i32 m0, s76, 0x2000
	s_nop 0
	global_load_lds_dwordx4 v[182:183], off
	v_lshl_add_u64 v[182:183], s[54:55], 0, v[162:163]
	s_mov_b32 m0, s51
	s_nop 0
	global_load_lds_dwordx4 v[182:183], off
	s_mov_b32 m0, s57
	s_nop 0
	global_load_lds_dwordx4 v[184:185], off
	s_waitcnt vmcnt(8)
	s_waitcnt lgkmcnt(0)
	s_barrier
	s_setprio 1
	s_nop 3
	s_waitcnt lgkmcnt(0)
	v_mfma_scale_f32_16x16x128_f8f6f4 v[94:97], v[26:33], v[196:203], v[94:97], v191, v192 op_sel_hi:[0,0,0]
	v_mfma_scale_f32_16x16x128_f8f6f4 v[90:93], v[18:25], v[196:203], v[90:93], v191, v192 op_sel_hi:[0,0,0]
	v_mfma_scale_f32_16x16x128_f8f6f4 v[78:81], v[26:33], v[204:211], v[78:81], v191, v192 op_sel_hi:[0,0,0]
	v_mfma_scale_f32_16x16x128_f8f6f4 v[74:77], v[18:25], v[204:211], v[74:77], v191, v192 op_sel_hi:[0,0,0]
	v_mfma_scale_f32_16x16x128_f8f6f4 v[62:65], v[26:33], v[212:219], v[62:65], v191, v192 op_sel_hi:[0,0,0]
	v_mfma_scale_f32_16x16x128_f8f6f4 v[58:61], v[18:25], v[212:219], v[58:61], v191, v192 op_sel_hi:[0,0,0]
	v_mfma_scale_f32_16x16x128_f8f6f4 v[46:49], v[26:33], v[220:227], v[46:49], v191, v192 op_sel_hi:[0,0,0]
	v_mfma_scale_f32_16x16x128_f8f6f4 v[42:45], v[18:25], v[220:227], v[42:45], v191, v192 op_sel_hi:[0,0,0]
	s_setprio 0
	s_setprio 1
	s_nop 3
	v_mfma_scale_f32_16x16x128_f8f6f4 v[86:89], v[10:17], v[196:203], v[86:89], v191, v192 op_sel_hi:[0,0,0]
	v_mfma_scale_f32_16x16x128_f8f6f4 v[82:85], v[2:9], v[196:203], v[82:85], v191, v192 op_sel_hi:[0,0,0]
	v_mfma_scale_f32_16x16x128_f8f6f4 v[70:73], v[10:17], v[204:211], v[70:73], v191, v192 op_sel_hi:[0,0,0]
	v_mfma_scale_f32_16x16x128_f8f6f4 v[66:69], v[2:9], v[204:211], v[66:69], v191, v192 op_sel_hi:[0,0,0]
	v_mfma_scale_f32_16x16x128_f8f6f4 v[54:57], v[10:17], v[212:219], v[54:57], v191, v192 op_sel_hi:[0,0,0]
	v_mfma_scale_f32_16x16x128_f8f6f4 v[50:53], v[2:9], v[212:219], v[50:53], v191, v192 op_sel_hi:[0,0,0]
	v_mfma_scale_f32_16x16x128_f8f6f4 v[38:41], v[10:17], v[220:227], v[38:41], v191, v192 op_sel_hi:[0,0,0]
	v_mfma_scale_f32_16x16x128_f8f6f4 v[34:37], v[2:9], v[220:227], v[34:37], v191, v192 op_sel_hi:[0,0,0]
	s_setprio 0
	s_barrier
; #define PG8_STAGE(bufoff, gbase, voff) do { _Pragma("unroll") for (int _i = 0; _i < 2; ++_i) \
;         __builtin_amdgcn_global_load_lds((const unsigned*)((const char*)(gbase) + (voff)[_i]), (PG8_LAS unsigned*)(lds + (bufoff) + ldsw + _i * 8192), 16, 0, 0); } while (0)
; #define PG8_STAGE_A(bufoff, gbase, h, nx) do { if constexpr (Sched::GATHER) { const unsigned vv_[2] = {(nx) ? vAn[h][0] : vA[h][0], (nx) ? vAn[h][1] : vA[h][1]}; PG8_STAGE(bufoff, gbase, vv_); } \
;         else { PG8_STAGE(bufoff, (gbase) + (h) * hstep, voffA); } } while (0)
; #define PG8_LDA(dst, b, h) do { _Pragma("unroll") for (int m = 0; m < 4; ++m) _Pragma("unroll") for (int k = 0; k < 2; ++k) dst[m][k] = *(const PG8_LAS bf16x8*)(lds + PG8_SA(b, h) + aoff + m * 2048 + k * 1024); } while (0)
; #define PG8_LDB(dst, b, h) do { _Pragma("unroll") for (int n = 0; n < 2; ++n) _Pragma("unroll") for (int k = 0; k < 2; ++k) dst[n][k] = *(const PG8_LAS bf16x8*)(lds + PG8_SB(b, h) + boff + n * 2048 + k * 1024); } while (0)
; #define PG8_WAIT_V(n) asm volatile("s_waitcnt vmcnt(" #n ")" ::: "memory")
; #define PG8_WAIT_L(n) asm volatile("s_waitcnt lgkmcnt(" #n ")" ::: "memory")
; #define PG8_BAR __builtin_amdgcn_s_barrier()
; #define PG8_SCHED __builtin_amdgcn_sched_barrier(0)
;     ...
;         for (int t = 0; t < nt; t += 2) {
;     ...
;             PG8_LDB(B0, 1, 0); PG8_LDB(B1, 1, 1); PG8_SCHED; PG8_LDA(At, 1, 0); PG8_STAGE_A(PG8_SA(0, 1), a2, 1, last);
;             PG8_WAIT_V(8); PG8_WAIT_L(0); PG8_BAR; PG8_MMA(0, 0, At, B0); PG8_MMA(0, 1, At, B1); PG8_BAR; PG8_SCHED;
;             PG8_LDA(At, 1, 1); PG8_STAGE(PG8_SB(1, 0), b3, voffB); PG8_STAGE(PG8_SB(1, 1), b3 + hstepB, voffB); PG8_STAGE_A(PG8_SA(1, 0), a3, 0, last);
;             PG8_WAIT_V(8); PG8_WAIT_L(0); PG8_BAR; PG8_MMA(1, 0, At, B0); PG8_MMA(1, 1, At, B1); PG8_BAR; PG8_SCHED;
	s_add_i32 s74, 0, 0x18000
	s_add_i32 s75, 0, 0x1c000
	v_add_u32_e32 v14, s74, v187
	v_add_u32_e32 v30, s75, v187
	ds_read_b128 v[2:5], v14
	ds_read_b128 v[6:9], v14 offset:1024
	ds_read_b128 v[10:13], v14 offset:2048
	ds_read_b128 v[14:17], v14 offset:3072
	ds_read_b128 v[18:21], v30
	ds_read_b128 v[22:25], v30 offset:1024
	ds_read_b128 v[26:29], v30 offset:2048
	ds_read_b128 v[30:33], v30 offset:3072
	s_add_u32 s54, s54, 0x20000
	s_addc_u32 s55, s55, 0
	s_mov_b32 m0, s58
	v_lshl_add_u64 v[228:229], s[54:55], 0, v[162:163]
	ds_read_b128 v[196:199], v190 offset:32768
	ds_read_b128 v[200:203], v190 offset:33792
	ds_read_b128 v[204:207], v190 offset:34816
	ds_read_b128 v[208:211], v190 offset:35840
	ds_read_b128 v[212:215], v190 offset:36864
	ds_read_b128 v[216:219], v190 offset:37888
	ds_read_b128 v[220:223], v190 offset:38912
	ds_read_b128 v[224:227], v190 offset:39936
	global_load_lds_dwordx4 v[228:229], off
	v_lshl_add_u64 v[228:229], s[54:55], 0, v[166:167]
	s_mov_b32 m0, s59
	s_nop 0
	global_load_lds_dwordx4 v[228:229], off
	s_waitcnt vmcnt(8)
	s_waitcnt lgkmcnt(0)
	s_barrier
	s_setprio 1
	s_nop 3
	s_waitcnt lgkmcnt(0)
	v_mfma_scale_f32_16x16x128_f8f6f4 v[158:161], v[2:9], v[196:203], v[158:161], v191, v192 op_sel_hi:[0,0,0]
	v_mfma_scale_f32_16x16x128_f8f6f4 v[154:157], v[10:17], v[196:203], v[154:157], v191, v192 op_sel_hi:[0,0,0]
	v_mfma_scale_f32_16x16x128_f8f6f4 v[142:145], v[2:9], v[204:211], v[142:145], v191, v192 op_sel_hi:[0,0,0]
	v_mfma_scale_f32_16x16x128_f8f6f4 v[138:141], v[10:17], v[204:211], v[138:141], v191, v192 op_sel_hi:[0,0,0]
	v_mfma_scale_f32_16x16x128_f8f6f4 v[126:129], v[2:9], v[212:219], v[126:129], v191, v192 op_sel_hi:[0,0,0]
	v_mfma_scale_f32_16x16x128_f8f6f4 v[122:125], v[10:17], v[212:219], v[122:125], v191, v192 op_sel_hi:[0,0,0]
	v_mfma_scale_f32_16x16x128_f8f6f4 v[110:113], v[2:9], v[220:227], v[110:113], v191, v192 op_sel_hi:[0,0,0]
	v_mfma_scale_f32_16x16x128_f8f6f4 v[106:109], v[10:17], v[220:227], v[106:109], v191, v192 op_sel_hi:[0,0,0]
	s_setprio 0
	s_setprio 1
	s_nop 3
	v_mfma_scale_f32_16x16x128_f8f6f4 v[150:153], v[18:25], v[196:203], v[150:153], v191, v192 op_sel_hi:[0,0,0]
	v_mfma_scale_f32_16x16x128_f8f6f4 v[146:149], v[26:33], v[196:203], v[146:149], v191, v192 op_sel_hi:[0,0,0]
	v_mfma_scale_f32_16x16x128_f8f6f4 v[134:137], v[18:25], v[204:211], v[134:137], v191, v192 op_sel_hi:[0,0,0]
	v_mfma_scale_f32_16x16x128_f8f6f4 v[130:133], v[26:33], v[204:211], v[130:133], v191, v192 op_sel_hi:[0,0,0]
	v_mfma_scale_f32_16x16x128_f8f6f4 v[118:121], v[18:25], v[212:219], v[118:121], v191, v192 op_sel_hi:[0,0,0]
	v_mfma_scale_f32_16x16x128_f8f6f4 v[114:117], v[26:33], v[212:219], v[114:117], v191, v192 op_sel_hi:[0,0,0]
	v_mfma_scale_f32_16x16x128_f8f6f4 v[102:105], v[18:25], v[220:227], v[102:105], v191, v192 op_sel_hi:[0,0,0]
	v_mfma_scale_f32_16x16x128_f8f6f4 v[98:101], v[26:33], v[220:227], v[98:101], v191, v192 op_sel_hi:[0,0,0]
	s_setprio 0
	s_barrier
	s_add_i32 s54, s74, s56
	v_lshl_add_u64 v[178:179], v[178:179], 0, s[18:19]
	s_mov_b32 m0, s54
	ds_read_b128 v[196:199], v190 offset:49152
	ds_read_b128 v[200:203], v190 offset:50176
	ds_read_b128 v[204:207], v190 offset:51200
	ds_read_b128 v[208:211], v190 offset:52224
	ds_read_b128 v[212:215], v190 offset:53248
	ds_read_b128 v[216:219], v190 offset:54272
	ds_read_b128 v[220:223], v190 offset:55296
	ds_read_b128 v[224:227], v190 offset:56320
	global_load_lds_dwordx4 v[178:179], off
	s_add_i32 m0, s54, 0x2000
	s_add_u32 s52, s52, 0x8080
	v_lshl_add_u64 v[178:179], v[180:181], 0, s[18:19]
	s_addc_u32 s53, s53, 0
	s_add_i32 s54, s75, s56
	global_load_lds_dwordx4 v[178:179], off
	v_lshl_add_u64 v[178:179], s[52:53], 0, v[164:165]
	s_mov_b32 m0, s54
	s_nop 0
	global_load_lds_dwordx4 v[178:179], off
	v_lshl_add_u64 v[178:179], s[52:53], 0, v[168:169]
	s_add_i32 m0, s54, 0x2000
	s_nop 0
	global_load_lds_dwordx4 v[178:179], off
	v_lshl_add_u64 v[178:179], v[182:183], 0, s[18:19]
	s_mov_b32 m0, s64
	s_nop 0
	global_load_lds_dwordx4 v[178:179], off
	v_lshl_add_u64 v[178:179], v[184:185], 0, s[18:19]
	s_mov_b32 m0, s65
	s_nop 0
	global_load_lds_dwordx4 v[178:179], off
	s_waitcnt vmcnt(8)
	s_waitcnt lgkmcnt(0)
	s_barrier
	s_setprio 1
	s_nop 3
	s_waitcnt lgkmcnt(0)
	v_mfma_scale_f32_16x16x128_f8f6f4 v[94:97], v[2:9], v[196:203], v[94:97], v191, v192 op_sel_hi:[0,0,0]
	v_mfma_scale_f32_16x16x128_f8f6f4 v[90:93], v[10:17], v[196:203], v[90:93], v191, v192 op_sel_hi:[0,0,0]
	v_mfma_scale_f32_16x16x128_f8f6f4 v[78:81], v[2:9], v[204:211], v[78:81], v191, v192 op_sel_hi:[0,0,0]
	v_mfma_scale_f32_16x16x128_f8f6f4 v[74:77], v[10:17], v[204:211], v[74:77], v191, v192 op_sel_hi:[0,0,0]
	v_mfma_scale_f32_16x16x128_f8f6f4 v[62:65], v[2:9], v[212:219], v[62:65], v191, v192 op_sel_hi:[0,0,0]
	v_mfma_scale_f32_16x16x128_f8f6f4 v[58:61], v[10:17], v[212:219], v[58:61], v191, v192 op_sel_hi:[0,0,0]
	v_mfma_scale_f32_16x16x128_f8f6f4 v[46:49], v[2:9], v[220:227], v[46:49], v191, v192 op_sel_hi:[0,0,0]
	v_mfma_scale_f32_16x16x128_f8f6f4 v[42:45], v[10:17], v[220:227], v[42:45], v191, v192 op_sel_hi:[0,0,0]
	s_setprio 0
	s_setprio 1
	s_nop 3
	v_mfma_scale_f32_16x16x128_f8f6f4 v[86:89], v[18:25], v[196:203], v[86:89], v191, v192 op_sel_hi:[0,0,0]
	v_mfma_scale_f32_16x16x128_f8f6f4 v[82:85], v[26:33], v[196:203], v[82:85], v191, v192 op_sel_hi:[0,0,0]
	v_mfma_scale_f32_16x16x128_f8f6f4 v[70:73], v[18:25], v[204:211], v[70:73], v191, v192 op_sel_hi:[0,0,0]
	v_mfma_scale_f32_16x16x128_f8f6f4 v[66:69], v[26:33], v[204:211], v[66:69], v191, v192 op_sel_hi:[0,0,0]
	v_mfma_scale_f32_16x16x128_f8f6f4 v[54:57], v[18:25], v[212:219], v[54:57], v191, v192 op_sel_hi:[0,0,0]
	v_mfma_scale_f32_16x16x128_f8f6f4 v[50:53], v[26:33], v[212:219], v[50:53], v191, v192 op_sel_hi:[0,0,0]
	v_mfma_scale_f32_16x16x128_f8f6f4 v[38:41], v[18:25], v[220:227], v[38:41], v191, v192 op_sel_hi:[0,0,0]
	v_mfma_scale_f32_16x16x128_f8f6f4 v[34:37], v[26:33], v[220:227], v[34:37], v191, v192 op_sel_hi:[0,0,0]
	s_setprio 0
	s_add_i32 s73, s73, 2
	s_add_u32 s6, s6, 0x100
	s_addc_u32 s7, s7, 0
	s_add_u32 s71, s71, 0x100
	s_addc_u32 s72, s72, 0
	s_cmp_gt_u32 s73, 5
	s_barrier
	s_cbranch_scc0 .LBB0_1026
	s_and_b64 vcc, exec, s[20:21]
	s_cbranch_vccz .LBB0_1029
	s_barrier

; #define PG8_STAGE(bufoff, gbase, voff) do { _Pragma("unroll") for (int _i = 0; _i < 2; ++_i) \
;         __builtin_amdgcn_global_load_lds((const unsigned*)((const char*)(gbase) + (voff)[_i]), (PG8_LAS unsigned*)(lds + (bufoff) + ldsw + _i * 8192), 16, 0, 0); } while (0)
; #define PG8_STAGE_A(bufoff, gbase, h, nx) do { if constexpr (Sched::GATHER) { const unsigned vv_[2] = {(nx) ? vAn[h][0] : vA[h][0], (nx) ? vAn[h][1] : vA[h][1]}; PG8_STAGE(bufoff, gbase, vv_); } \
;         else { PG8_STAGE(bufoff, (gbase) + (h) * hstep, voffA); } } while (0)
; #define PG8_LDA(dst, b, h) do { _Pragma("unroll") for (int m = 0; m < 4; ++m) _Pragma("unroll") for (int k = 0; k < 2; ++k) dst[m][k] = *(const PG8_LAS bf16x8*)(lds + PG8_SA(b, h) + aoff + m * 2048 + k * 1024); } while (0)
; #define PG8_LDB(dst, b, h) do { _Pragma("unroll") for (int n = 0; n < 2; ++n) _Pragma("unroll") for (int k = 0; k < 2; ++k) dst[n][k] = *(const PG8_LAS bf16x8*)(lds + PG8_SB(b, h) + boff + n * 2048 + k * 1024); } while (0)
; #define PG8_WAIT_V(n) asm volatile("s_waitcnt vmcnt(" #n ")" ::: "memory")
; #define PG8_WAIT_L(n) asm volatile("s_waitcnt lgkmcnt(" #n ")" ::: "memory")
; #define PG8_BAR __builtin_amdgcn_s_barrier()
; #define PG8_SCHED __builtin_amdgcn_sched_barrier(0)
;     ...
;         for (int t = 0; t < nt; t += 2) {
;             const bool last = (t == nt - 2);
;             const char* a1 = cA + (size_t)(t + 1) * kstep;
;             const char* a2 = last ? nA : cA + (size_t)(t + 2) * kstep; const char* b2 = last ? nB : cB + (size_t)(t + 2) * kstep;
;             const char* a3 = a2 + kstep; const char* b3 = b2 + kstep;
;             if (last && has_next) S.a_ready(nxt);
;             if constexpr (SP2) {
;             PG8_LDB(B0, 0, 0); PG8_LDB(B1, 0, 1); PG8_SCHED; PG8_LDA(At, 0, 0); PG8_STAGE_A(PG8_SA(1, 1), a1, 1, false);
;             PG8_WAIT_V(8); PG8_WAIT_L(0); PG8_BAR; PG8_MMA(0, 0, At, B0); PG8_MMA(0, 1, At, B1); PG8_BAR; PG8_SCHED;
;             PG8_LDA(At, 0, 1); PG8_STAGE(PG8_SB(0, 0), b2, voffB); PG8_STAGE(PG8_SB(0, 1), b2 + hstepB, voffB); PG8_STAGE_A(PG8_SA(0, 0), a2, 0, last);
;             PG8_WAIT_V(8); PG8_WAIT_L(0); PG8_BAR; PG8_MMA(1, 0, At, B0); PG8_MMA(1, 1, At, B1); PG8_BAR; PG8_SCHED;
.LBB0_1205:
	ds_read_b128 v[26:29], v188
	ds_read_b128 v[30:33], v188 offset:1024
	ds_read_b128 v[18:21], v188 offset:2048
	ds_read_b128 v[22:25], v188 offset:3072
	ds_read_b128 v[10:13], v189
	ds_read_b128 v[14:17], v189 offset:1024
	ds_read_b128 v[2:5], v189 offset:2048
	ds_read_b128 v[6:9], v189 offset:3072
	s_add_u32 s26, s24, 0xfffe0080
	s_addc_u32 s27, s25, -1
	s_cmp_eq_u32 s48, 4
	s_cselect_b32 s29, s17, s27
	s_cselect_b32 s28, s44, s26
	s_cselect_b32 s27, s15, s47
	s_cselect_b32 s26, s45, s46
	v_lshl_add_u64 v[218:219], s[24:25], 0, v[170:171]
	s_add_i32 m0, s23, 0xc000
	ds_read_b128 v[178:181], v190
	ds_read_b128 v[182:185], v190 offset:1024
	ds_read_b128 v[194:197], v190 offset:2048
	ds_read_b128 v[198:201], v190 offset:3072
	ds_read_b128 v[202:205], v190 offset:4096
	ds_read_b128 v[206:209], v190 offset:5120
	ds_read_b128 v[210:213], v190 offset:6144
	ds_read_b128 v[214:217], v190 offset:7168
	global_load_lds_dwordx4 v[218:219], off
	v_lshl_add_u64 v[218:219], s[24:25], 0, v[172:173]
	s_add_i32 m0, s23, 0xe000
	s_nop 0
	global_load_lds_dwordx4 v[218:219], off
	s_waitcnt vmcnt(8)
	s_waitcnt lgkmcnt(0)
	s_barrier
	s_setprio 1
	s_nop 3
	s_waitcnt lgkmcnt(0)
	v_mfma_scale_f32_16x16x128_f8f6f4 v[158:161], v[26:33], v[178:185], v[158:161], v191, v192 op_sel_hi:[0,0,0]
	v_mfma_scale_f32_16x16x128_f8f6f4 v[154:157], v[18:25], v[178:185], v[154:157], v191, v192 op_sel_hi:[0,0,0]
	v_mfma_scale_f32_16x16x128_f8f6f4 v[142:145], v[26:33], v[194:201], v[142:145], v191, v192 op_sel_hi:[0,0,0]
	v_mfma_scale_f32_16x16x128_f8f6f4 v[138:141], v[18:25], v[194:201], v[138:141], v191, v192 op_sel_hi:[0,0,0]
	v_mfma_scale_f32_16x16x128_f8f6f4 v[126:129], v[26:33], v[202:209], v[126:129], v191, v192 op_sel_hi:[0,0,0]
	v_mfma_scale_f32_16x16x128_f8f6f4 v[122:125], v[18:25], v[202:209], v[122:125], v191, v192 op_sel_hi:[0,0,0]
	v_mfma_scale_f32_16x16x128_f8f6f4 v[110:113], v[26:33], v[210:217], v[110:113], v191, v192 op_sel_hi:[0,0,0]
	v_mfma_scale_f32_16x16x128_f8f6f4 v[106:109], v[18:25], v[210:217], v[106:109], v191, v192 op_sel_hi:[0,0,0]
	s_setprio 0
	s_setprio 1
	s_nop 3
	v_mfma_scale_f32_16x16x128_f8f6f4 v[150:153], v[10:17], v[178:185], v[150:153], v191, v192 op_sel_hi:[0,0,0]
	v_mfma_scale_f32_16x16x128_f8f6f4 v[146:149], v[2:9], v[178:185], v[146:149], v191, v192 op_sel_hi:[0,0,0]
	v_mfma_scale_f32_16x16x128_f8f6f4 v[134:137], v[10:17], v[194:201], v[134:137], v191, v192 op_sel_hi:[0,0,0]
	v_mfma_scale_f32_16x16x128_f8f6f4 v[130:133], v[2:9], v[194:201], v[130:133], v191, v192 op_sel_hi:[0,0,0]
	v_mfma_scale_f32_16x16x128_f8f6f4 v[118:121], v[10:17], v[202:209], v[118:121], v191, v192 op_sel_hi:[0,0,0]
	v_mfma_scale_f32_16x16x128_f8f6f4 v[114:117], v[2:9], v[202:209], v[114:117], v191, v192 op_sel_hi:[0,0,0]
	v_mfma_scale_f32_16x16x128_f8f6f4 v[102:105], v[10:17], v[210:217], v[102:105], v191, v192 op_sel_hi:[0,0,0]
	v_mfma_scale_f32_16x16x128_f8f6f4 v[98:101], v[2:9], v[210:217], v[98:101], v191, v192 op_sel_hi:[0,0,0]
	s_setprio 0
	s_barrier
	s_add_i32 s49, s41, s30
	v_lshl_add_u64 v[178:179], s[26:27], 0, v[164:165]
	s_mov_b32 m0, s49
	ds_read_b128 v[194:197], v190 offset:16384
	ds_read_b128 v[198:201], v190 offset:17408
	ds_read_b128 v[202:205], v190 offset:18432
	ds_read_b128 v[206:209], v190 offset:19456
	ds_read_b128 v[210:213], v190 offset:20480
	ds_read_b128 v[214:217], v190 offset:21504
	ds_read_b128 v[218:221], v190 offset:22528
	ds_read_b128 v[222:225], v190 offset:23552
	global_load_lds_dwordx4 v[178:179], off
	s_add_i32 m0, s49, 0x2000
	s_add_u32 s50, s26, 0x2000
	v_lshl_add_u64 v[180:181], s[26:27], 0, v[168:169]
	s_addc_u32 s51, s27, 0
	s_add_i32 s49, s42, s30
	global_load_lds_dwordx4 v[180:181], off
	v_lshl_add_u64 v[182:183], s[50:51], 0, v[164:165]
	s_mov_b32 m0, s49
	v_lshl_add_u64 v[184:185], s[28:29], 0, v[166:167]
	global_load_lds_dwordx4 v[182:183], off
	v_lshl_add_u64 v[182:183], s[50:51], 0, v[168:169]
	s_add_i32 m0, s49, 0x2000
	s_nop 0
	global_load_lds_dwordx4 v[182:183], off
	v_lshl_add_u64 v[182:183], s[28:29], 0, v[162:163]
	s_mov_b32 m0, s23
	s_nop 0
	global_load_lds_dwordx4 v[182:183], off
	s_mov_b32 m0, s34
	s_nop 0
	global_load_lds_dwordx4 v[184:185], off
	s_waitcnt vmcnt(8)
	s_waitcnt lgkmcnt(0)
	s_barrier
	s_setprio 1
	s_nop 3
	s_waitcnt lgkmcnt(0)
	v_mfma_scale_f32_16x16x128_f8f6f4 v[94:97], v[26:33], v[194:201], v[94:97], v191, v192 op_sel_hi:[0,0,0]
	v_mfma_scale_f32_16x16x128_f8f6f4 v[90:93], v[18:25], v[194:201], v[90:93], v191, v192 op_sel_hi:[0,0,0]
	v_mfma_scale_f32_16x16x128_f8f6f4 v[78:81], v[26:33], v[202:209], v[78:81], v191, v192 op_sel_hi:[0,0,0]
	v_mfma_scale_f32_16x16x128_f8f6f4 v[74:77], v[18:25], v[202:209], v[74:77], v191, v192 op_sel_hi:[0,0,0]
	v_mfma_scale_f32_16x16x128_f8f6f4 v[62:65], v[26:33], v[210:217], v[62:65], v191, v192 op_sel_hi:[0,0,0]
	v_mfma_scale_f32_16x16x128_f8f6f4 v[58:61], v[18:25], v[210:217], v[58:61], v191, v192 op_sel_hi:[0,0,0]
	v_mfma_scale_f32_16x16x128_f8f6f4 v[46:49], v[26:33], v[218:225], v[46:49], v191, v192 op_sel_hi:[0,0,0]
	v_mfma_scale_f32_16x16x128_f8f6f4 v[42:45], v[18:25], v[218:225], v[42:45], v191, v192 op_sel_hi:[0,0,0]
	s_setprio 0
	s_setprio 1
	s_nop 3
	v_mfma_scale_f32_16x16x128_f8f6f4 v[86:89], v[10:17], v[194:201], v[86:89], v191, v192 op_sel_hi:[0,0,0]
	v_mfma_scale_f32_16x16x128_f8f6f4 v[82:85], v[2:9], v[194:201], v[82:85], v191, v192 op_sel_hi:[0,0,0]
	v_mfma_scale_f32_16x16x128_f8f6f4 v[70:73], v[10:17], v[202:209], v[70:73], v191, v192 op_sel_hi:[0,0,0]
	v_mfma_scale_f32_16x16x128_f8f6f4 v[66:69], v[2:9], v[202:209], v[66:69], v191, v192 op_sel_hi:[0,0,0]
	v_mfma_scale_f32_16x16x128_f8f6f4 v[54:57], v[10:17], v[210:217], v[54:57], v191, v192 op_sel_hi:[0,0,0]
	v_mfma_scale_f32_16x16x128_f8f6f4 v[50:53], v[2:9], v[210:217], v[50:53], v191, v192 op_sel_hi:[0,0,0]
	v_mfma_scale_f32_16x16x128_f8f6f4 v[38:41], v[10:17], v[218:225], v[38:41], v191, v192 op_sel_hi:[0,0,0]
	v_mfma_scale_f32_16x16x128_f8f6f4 v[34:37], v[2:9], v[218:225], v[34:37], v191, v192 op_sel_hi:[0,0,0]
	s_setprio 0
	s_barrier
; #define PG8_STAGE(bufoff, gbase, voff) do { _Pragma("unroll") for (int _i = 0; _i < 2; ++_i) \
;         __builtin_amdgcn_global_load_lds((const unsigned*)((const char*)(gbase) + (voff)[_i]), (PG8_LAS unsigned*)(lds + (bufoff) + ldsw + _i * 8192), 16, 0, 0); } while (0)
; #define PG8_STAGE_A(bufoff, gbase, h, nx) do { if constexpr (Sched::GATHER) { const unsigned vv_[2] = {(nx) ? vAn[h][0] : vA[h][0], (nx) ? vAn[h][1] : vA[h][1]}; PG8_STAGE(bufoff, gbase, vv_); } \
;         else { PG8_STAGE(bufoff, (gbase) + (h) * hstep, voffA); } } while (0)
; #define PG8_LDA(dst, b, h) do { _Pragma("unroll") for (int m = 0; m < 4; ++m) _Pragma("unroll") for (int k = 0; k < 2; ++k) dst[m][k] = *(const PG8_LAS bf16x8*)(lds + PG8_SA(b, h) + aoff + m * 2048 + k * 1024); } while (0)
; #define PG8_LDB(dst, b, h) do { _Pragma("unroll") for (int n = 0; n < 2; ++n) _Pragma("unroll") for (int k = 0; k < 2; ++k) dst[n][k] = *(const PG8_LAS bf16x8*)(lds + PG8_SB(b, h) + boff + n * 2048 + k * 1024); } while (0)
; #define PG8_WAIT_V(n) asm volatile("s_waitcnt vmcnt(" #n ")" ::: "memory")
; #define PG8_WAIT_L(n) asm volatile("s_waitcnt lgkmcnt(" #n ")" ::: "memory")
; #define PG8_BAR __builtin_amdgcn_s_barrier()
; #define PG8_SCHED __builtin_amdgcn_sched_barrier(0)
;     ...
;         for (int t = 0; t < nt; t += 2) {
;     ...
;             PG8_LDB(B0, 1, 0); PG8_LDB(B1, 1, 1); PG8_SCHED; PG8_LDA(At, 1, 0); PG8_STAGE_A(PG8_SA(0, 1), a2, 1, last);
;             PG8_WAIT_V(8); PG8_WAIT_L(0); PG8_BAR; PG8_MMA(0, 0, At, B0); PG8_MMA(0, 1, At, B1); PG8_BAR; PG8_SCHED;
;             PG8_LDA(At, 1, 1); PG8_STAGE(PG8_SB(1, 0), b3, voffB); PG8_STAGE(PG8_SB(1, 1), b3 + hstepB, voffB); PG8_STAGE_A(PG8_SA(1, 0), a3, 0, last);
;             PG8_WAIT_V(8); PG8_WAIT_L(0); PG8_BAR; PG8_MMA(1, 0, At, B0); PG8_MMA(1, 1, At, B1); PG8_BAR; PG8_SCHED;
	s_add_i32 s49, 0, 0x18000
	s_add_i32 s50, 0, 0x1c000
	v_add_u32_e32 v14, s49, v186
	v_add_u32_e32 v30, s50, v186
	ds_read_b128 v[2:5], v14
	ds_read_b128 v[6:9], v14 offset:1024
	ds_read_b128 v[10:13], v14 offset:2048
	ds_read_b128 v[14:17], v14 offset:3072
	ds_read_b128 v[18:21], v30
	ds_read_b128 v[22:25], v30 offset:1024
	ds_read_b128 v[26:29], v30 offset:2048
	ds_read_b128 v[30:33], v30 offset:3072
	s_add_u32 s28, s28, 0x20000
	s_addc_u32 s29, s29, 0
	s_mov_b32 m0, s35
	v_lshl_add_u64 v[226:227], s[28:29], 0, v[162:163]
	ds_read_b128 v[194:197], v190 offset:32768
	ds_read_b128 v[198:201], v190 offset:33792
	ds_read_b128 v[202:205], v190 offset:34816
	ds_read_b128 v[206:209], v190 offset:35840
	ds_read_b128 v[210:213], v190 offset:36864
	ds_read_b128 v[214:217], v190 offset:37888
	ds_read_b128 v[218:221], v190 offset:38912
	ds_read_b128 v[222:225], v190 offset:39936
	global_load_lds_dwordx4 v[226:227], off
	v_lshl_add_u64 v[226:227], s[28:29], 0, v[166:167]
	s_mov_b32 m0, s36
	s_nop 0
	global_load_lds_dwordx4 v[226:227], off
	s_waitcnt vmcnt(8)
	s_waitcnt lgkmcnt(0)
	s_barrier
	s_setprio 1
	s_nop 3
	s_waitcnt lgkmcnt(0)
	v_mfma_scale_f32_16x16x128_f8f6f4 v[158:161], v[2:9], v[194:201], v[158:161], v191, v192 op_sel_hi:[0,0,0]
	v_mfma_scale_f32_16x16x128_f8f6f4 v[154:157], v[10:17], v[194:201], v[154:157], v191, v192 op_sel_hi:[0,0,0]
	v_mfma_scale_f32_16x16x128_f8f6f4 v[142:145], v[2:9], v[202:209], v[142:145], v191, v192 op_sel_hi:[0,0,0]
	v_mfma_scale_f32_16x16x128_f8f6f4 v[138:141], v[10:17], v[202:209], v[138:141], v191, v192 op_sel_hi:[0,0,0]
	v_mfma_scale_f32_16x16x128_f8f6f4 v[126:129], v[2:9], v[210:217], v[126:129], v191, v192 op_sel_hi:[0,0,0]
	v_mfma_scale_f32_16x16x128_f8f6f4 v[122:125], v[10:17], v[210:217], v[122:125], v191, v192 op_sel_hi:[0,0,0]
	v_mfma_scale_f32_16x16x128_f8f6f4 v[110:113], v[2:9], v[218:225], v[110:113], v191, v192 op_sel_hi:[0,0,0]
	v_mfma_scale_f32_16x16x128_f8f6f4 v[106:109], v[10:17], v[218:225], v[106:109], v191, v192 op_sel_hi:[0,0,0]
	s_setprio 0
	s_setprio 1
	s_nop 3
	v_mfma_scale_f32_16x16x128_f8f6f4 v[150:153], v[18:25], v[194:201], v[150:153], v191, v192 op_sel_hi:[0,0,0]
	v_mfma_scale_f32_16x16x128_f8f6f4 v[146:149], v[26:33], v[194:201], v[146:149], v191, v192 op_sel_hi:[0,0,0]
	v_mfma_scale_f32_16x16x128_f8f6f4 v[134:137], v[18:25], v[202:209], v[134:137], v191, v192 op_sel_hi:[0,0,0]
	v_mfma_scale_f32_16x16x128_f8f6f4 v[130:133], v[26:33], v[202:209], v[130:133], v191, v192 op_sel_hi:[0,0,0]
	v_mfma_scale_f32_16x16x128_f8f6f4 v[118:121], v[18:25], v[210:217], v[118:121], v191, v192 op_sel_hi:[0,0,0]
	v_mfma_scale_f32_16x16x128_f8f6f4 v[114:117], v[26:33], v[210:217], v[114:117], v191, v192 op_sel_hi:[0,0,0]
	v_mfma_scale_f32_16x16x128_f8f6f4 v[102:105], v[18:25], v[218:225], v[102:105], v191, v192 op_sel_hi:[0,0,0]
	v_mfma_scale_f32_16x16x128_f8f6f4 v[98:101], v[26:33], v[218:225], v[98:101], v191, v192 op_sel_hi:[0,0,0]
	s_setprio 0
	s_barrier
	s_add_i32 s28, s49, s30
	v_lshl_add_u64 v[178:179], v[178:179], 0, s[8:9]
	s_mov_b32 m0, s28
	ds_read_b128 v[194:197], v190 offset:49152
	ds_read_b128 v[198:201], v190 offset:50176
	ds_read_b128 v[202:205], v190 offset:51200
	ds_read_b128 v[206:209], v190 offset:52224
	ds_read_b128 v[210:213], v190 offset:53248
	ds_read_b128 v[214:217], v190 offset:54272
	ds_read_b128 v[218:221], v190 offset:55296
	ds_read_b128 v[222:225], v190 offset:56320
	global_load_lds_dwordx4 v[178:179], off
	s_add_i32 m0, s28, 0x2000
	s_add_u32 s26, s26, 0x2080
	v_lshl_add_u64 v[178:179], v[180:181], 0, s[8:9]
	s_addc_u32 s27, s27, 0
	s_add_i32 s28, s50, s30
	global_load_lds_dwordx4 v[178:179], off
	v_lshl_add_u64 v[178:179], s[26:27], 0, v[164:165]
	s_mov_b32 m0, s28
	s_nop 0
	global_load_lds_dwordx4 v[178:179], off
	v_lshl_add_u64 v[178:179], s[26:27], 0, v[168:169]
	s_add_i32 m0, s28, 0x2000
	s_nop 0
	global_load_lds_dwordx4 v[178:179], off
	v_lshl_add_u64 v[178:179], v[182:183], 0, s[8:9]
	s_mov_b32 m0, s39
	s_nop 0
	global_load_lds_dwordx4 v[178:179], off
	v_lshl_add_u64 v[178:179], v[184:185], 0, s[8:9]
	s_mov_b32 m0, s40
	s_nop 0
	global_load_lds_dwordx4 v[178:179], off
	s_waitcnt vmcnt(8)
	s_waitcnt lgkmcnt(0)
	s_barrier
	s_setprio 1
	s_nop 3
	s_waitcnt lgkmcnt(0)
	v_mfma_scale_f32_16x16x128_f8f6f4 v[94:97], v[2:9], v[194:201], v[94:97], v191, v192 op_sel_hi:[0,0,0]
	v_mfma_scale_f32_16x16x128_f8f6f4 v[90:93], v[10:17], v[194:201], v[90:93], v191, v192 op_sel_hi:[0,0,0]
	v_mfma_scale_f32_16x16x128_f8f6f4 v[78:81], v[2:9], v[202:209], v[78:81], v191, v192 op_sel_hi:[0,0,0]
	v_mfma_scale_f32_16x16x128_f8f6f4 v[74:77], v[10:17], v[202:209], v[74:77], v191, v192 op_sel_hi:[0,0,0]
	v_mfma_scale_f32_16x16x128_f8f6f4 v[62:65], v[2:9], v[210:217], v[62:65], v191, v192 op_sel_hi:[0,0,0]
	v_mfma_scale_f32_16x16x128_f8f6f4 v[58:61], v[10:17], v[210:217], v[58:61], v191, v192 op_sel_hi:[0,0,0]
	v_mfma_scale_f32_16x16x128_f8f6f4 v[46:49], v[2:9], v[218:225], v[46:49], v191, v192 op_sel_hi:[0,0,0]
	v_mfma_scale_f32_16x16x128_f8f6f4 v[42:45], v[10:17], v[218:225], v[42:45], v191, v192 op_sel_hi:[0,0,0]
	s_setprio 0
	s_setprio 1
	s_nop 3
	v_mfma_scale_f32_16x16x128_f8f6f4 v[86:89], v[18:25], v[194:201], v[86:89], v191, v192 op_sel_hi:[0,0,0]
	v_mfma_scale_f32_16x16x128_f8f6f4 v[82:85], v[26:33], v[194:201], v[82:85], v191, v192 op_sel_hi:[0,0,0]
	v_mfma_scale_f32_16x16x128_f8f6f4 v[70:73], v[18:25], v[202:209], v[70:73], v191, v192 op_sel_hi:[0,0,0]
	v_mfma_scale_f32_16x16x128_f8f6f4 v[66:69], v[26:33], v[202:209], v[66:69], v191, v192 op_sel_hi:[0,0,0]
	v_mfma_scale_f32_16x16x128_f8f6f4 v[54:57], v[18:25], v[210:217], v[54:57], v191, v192 op_sel_hi:[0,0,0]
	v_mfma_scale_f32_16x16x128_f8f6f4 v[50:53], v[26:33], v[210:217], v[50:53], v191, v192 op_sel_hi:[0,0,0]
	v_mfma_scale_f32_16x16x128_f8f6f4 v[38:41], v[18:25], v[218:225], v[38:41], v191, v192 op_sel_hi:[0,0,0]
	v_mfma_scale_f32_16x16x128_f8f6f4 v[34:37], v[26:33], v[218:225], v[34:37], v191, v192 op_sel_hi:[0,0,0]
	s_setprio 0
	s_add_i32 s48, s48, 2
	s_add_u32 s24, s24, 0x100
	s_addc_u32 s25, s25, 0
	s_add_u32 s46, s46, 0x100
	s_addc_u32 s47, s47, 0
	s_cmp_gt_u32 s48, 5
	s_barrier
	s_cbranch_scc0 .LBB0_1205
	s_and_b64 vcc, exec, s[10:11]
	s_cbranch_vccz .LBB0_1208
	s_barrier

; #define PG8_STAGE(bufoff, gbase, voff) do { _Pragma("unroll") for (int _i = 0; _i < 2; ++_i) \
;         __builtin_amdgcn_global_load_lds((const unsigned*)((const char*)(gbase) + (voff)[_i]), (PG8_LAS unsigned*)(lds + (bufoff) + ldsw + _i * 8192), 16, 0, 0); } while (0)
; #define PG8_STAGE_A(bufoff, gbase, h, nx) do { if constexpr (Sched::GATHER) { const unsigned vv_[2] = {(nx) ? vAn[h][0] : vA[h][0], (nx) ? vAn[h][1] : vA[h][1]}; PG8_STAGE(bufoff, gbase, vv_); } \
;         else { PG8_STAGE(bufoff, (gbase) + (h) * hstep, voffA); } } while (0)
; #define PG8_LDA(dst, b, h) do { _Pragma("unroll") for (int m = 0; m < 4; ++m) _Pragma("unroll") for (int k = 0; k < 2; ++k) dst[m][k] = *(const PG8_LAS bf16x8*)(lds + PG8_SA(b, h) + aoff + m * 2048 + k * 1024); } while (0)
; #define PG8_LDB(dst, b, h) do { _Pragma("unroll") for (int n = 0; n < 2; ++n) _Pragma("unroll") for (int k = 0; k < 2; ++k) dst[n][k] = *(const PG8_LAS bf16x8*)(lds + PG8_SB(b, h) + boff + n * 2048 + k * 1024); } while (0)
; #define PG8_WAIT_V(n) asm volatile("s_waitcnt vmcnt(" #n ")" ::: "memory")
; #define PG8_WAIT_L(n) asm volatile("s_waitcnt lgkmcnt(" #n ")" ::: "memory")
; #define PG8_BAR __builtin_amdgcn_s_barrier()
; #define PG8_SCHED __builtin_amdgcn_sched_barrier(0)
;     ...
;             PG8_LDB(B0, 0, 0); PG8_LDB(B1, 0, 1); PG8_SCHED; PG8_LDA(At, 0, 0); PG8_STAGE_A(PG8_SA(1, 1), a1, 1, false);
;             PG8_WAIT_V(8); PG8_WAIT_L(0); PG8_BAR; PG8_MMA(0, 0, At, B0); PG8_MMA(0, 1, At, B1); PG8_BAR; PG8_SCHED;
;             PG8_LDA(At, 0, 1); PG8_STAGE(PG8_SB(0, 0), b2, voffB); PG8_STAGE(PG8_SB(0, 1), b2 + hstepB, voffB); PG8_STAGE_A(PG8_SA(0, 0), a2, 0, last);
;             PG8_WAIT_V(8); PG8_WAIT_L(0); PG8_BAR; PG8_MMA(1, 0, At, B0); PG8_MMA(1, 1, At, B1); PG8_BAR; PG8_SCHED;
.LBB0_1572:
	ds_read_b128 v[26:29], v194
	ds_read_b128 v[30:33], v194 offset:1024
	ds_read_b128 v[18:21], v194 offset:2048
	ds_read_b128 v[22:25], v194 offset:3072
	ds_read_b128 v[10:13], v195
	ds_read_b128 v[14:17], v195 offset:1024
	ds_read_b128 v[2:5], v195 offset:2048
	ds_read_b128 v[6:9], v195 offset:3072
	s_add_u32 s20, s58, s4
	s_addc_u32 s21, s59, s5
	s_add_u32 s22, s20, 0x25400100
	s_addc_u32 s23, s21, 0
	s_add_u32 s55, s52, s4
	s_addc_u32 s56, s53, s5
	s_cmpk_eq_i32 s4, 0x300
	s_cselect_b64 vcc, -1, 0
	s_and_b64 s[20:21], vcc, exec
	s_cselect_b32 s23, s93, s23
	s_cselect_b32 s22, s92, s22
	s_cselect_b32 s21, s17, s56
	s_cselect_b32 s20, s51, s55
	s_mov_b32 m0, s39
	v_lshl_add_u64 v[232:233], v[180:181], 0, s[4:5]
	ds_read_b128 v[182:185], v196
	ds_read_b128 v[186:189], v196 offset:1024
	ds_read_b128 v[208:211], v196 offset:2048
	ds_read_b128 v[212:215], v196 offset:3072
	ds_read_b128 v[216:219], v196 offset:4096
	ds_read_b128 v[220:223], v196 offset:5120
	ds_read_b128 v[224:227], v196 offset:6144
	ds_read_b128 v[228:231], v196 offset:7168
	global_load_lds_dwordx4 v[232:233], off
	v_lshl_add_u64 v[232:233], v[178:179], 0, s[4:5]
	s_mov_b32 m0, s40
	s_nop 0
	global_load_lds_dwordx4 v[232:233], off
	s_waitcnt vmcnt(8)
	s_waitcnt lgkmcnt(0)
	s_barrier
	s_setprio 1
	s_nop 3
	s_waitcnt lgkmcnt(0)
	v_mfma_scale_f32_16x16x128_f8f6f4 v[158:161], v[26:33], v[182:189], v[158:161], v197, v198 op_sel_hi:[0,0,0]
	v_mfma_scale_f32_16x16x128_f8f6f4 v[150:153], v[18:25], v[182:189], v[150:153], v197, v198 op_sel_hi:[0,0,0]
	v_mfma_scale_f32_16x16x128_f8f6f4 v[142:145], v[26:33], v[208:215], v[142:145], v197, v198 op_sel_hi:[0,0,0]
	v_mfma_scale_f32_16x16x128_f8f6f4 v[134:137], v[18:25], v[208:215], v[134:137], v197, v198 op_sel_hi:[0,0,0]
	v_mfma_scale_f32_16x16x128_f8f6f4 v[126:129], v[26:33], v[216:223], v[126:129], v197, v198 op_sel_hi:[0,0,0]
	v_mfma_scale_f32_16x16x128_f8f6f4 v[118:121], v[18:25], v[216:223], v[118:121], v197, v198 op_sel_hi:[0,0,0]
	v_mfma_scale_f32_16x16x128_f8f6f4 v[110:113], v[26:33], v[224:231], v[110:113], v197, v198 op_sel_hi:[0,0,0]
	v_mfma_scale_f32_16x16x128_f8f6f4 v[98:101], v[18:25], v[224:231], v[98:101], v197, v198 op_sel_hi:[0,0,0]
	s_setprio 0
	s_setprio 1
	s_nop 3
	v_mfma_scale_f32_16x16x128_f8f6f4 v[154:157], v[10:17], v[182:189], v[154:157], v197, v198 op_sel_hi:[0,0,0]
	v_mfma_scale_f32_16x16x128_f8f6f4 v[146:149], v[2:9], v[182:189], v[146:149], v197, v198 op_sel_hi:[0,0,0]
	v_mfma_scale_f32_16x16x128_f8f6f4 v[138:141], v[10:17], v[208:215], v[138:141], v197, v198 op_sel_hi:[0,0,0]
	v_mfma_scale_f32_16x16x128_f8f6f4 v[130:133], v[2:9], v[208:215], v[130:133], v197, v198 op_sel_hi:[0,0,0]
	v_mfma_scale_f32_16x16x128_f8f6f4 v[122:125], v[10:17], v[216:223], v[122:125], v197, v198 op_sel_hi:[0,0,0]
	v_mfma_scale_f32_16x16x128_f8f6f4 v[114:117], v[2:9], v[216:223], v[114:117], v197, v198 op_sel_hi:[0,0,0]
	v_mfma_scale_f32_16x16x128_f8f6f4 v[106:109], v[10:17], v[224:231], v[106:109], v197, v198 op_sel_hi:[0,0,0]
	v_mfma_scale_f32_16x16x128_f8f6f4 v[94:97], v[2:9], v[224:231], v[94:97], v197, v198 op_sel_hi:[0,0,0]
	s_setprio 0
	s_barrier
	s_mov_b32 m0, s41
	v_lshl_add_u64 v[182:183], s[20:21], 0, v[164:165]
	s_add_u32 s56, s20, 0x20000
	ds_read_b128 v[208:211], v196 offset:16384
	ds_read_b128 v[212:215], v196 offset:17408
	ds_read_b128 v[216:219], v196 offset:18432
	ds_read_b128 v[220:223], v196 offset:19456
	ds_read_b128 v[224:227], v196 offset:20480
	ds_read_b128 v[228:231], v196 offset:21504
	ds_read_b128 v[232:235], v196 offset:22528
	ds_read_b128 v[236:239], v196 offset:23552
	global_load_lds_dwordx4 v[182:183], off
	v_lshl_add_u64 v[184:185], s[20:21], 0, v[162:163]
	s_mov_b32 m0, s42
	s_addc_u32 s57, s21, 0
	global_load_lds_dwordx4 v[184:185], off
	v_lshl_add_u64 v[186:187], s[56:57], 0, v[164:165]
	s_mov_b32 m0, s43
	v_cndmask_b32_e32 v166, v206, v202, vcc
	global_load_lds_dwordx4 v[186:187], off
	v_lshl_add_u64 v[186:187], s[56:57], 0, v[162:163]
	s_mov_b32 m0, s44
	v_lshl_add_u64 v[188:189], s[22:23], 0, v[166:167]
	global_load_lds_dwordx4 v[186:187], off
	s_mov_b32 m0, s26
	v_cndmask_b32_e32 v186, v172, v203, vcc
	global_load_lds_dwordx4 v166, s[22:23]
	s_mov_b32 m0, s27
	v_mov_b32_e32 v187, v167
	global_load_lds_dwordx4 v186, s[22:23]
	s_waitcnt vmcnt(8)
	s_waitcnt lgkmcnt(0)
	v_lshl_add_u64 v[186:187], s[22:23], 0, v[186:187]
	s_barrier
	s_setprio 1
	s_nop 3
	s_waitcnt lgkmcnt(0)
	v_mfma_scale_f32_16x16x128_f8f6f4 v[82:85], v[26:33], v[208:215], v[82:85], v197, v198 op_sel_hi:[0,0,0]
	v_mfma_scale_f32_16x16x128_f8f6f4 v[70:73], v[18:25], v[208:215], v[70:73], v197, v198 op_sel_hi:[0,0,0]
	v_mfma_scale_f32_16x16x128_f8f6f4 v[78:81], v[26:33], v[216:223], v[78:81], v197, v198 op_sel_hi:[0,0,0]
	v_mfma_scale_f32_16x16x128_f8f6f4 v[66:69], v[18:25], v[216:223], v[66:69], v197, v198 op_sel_hi:[0,0,0]
	v_mfma_scale_f32_16x16x128_f8f6f4 v[58:61], v[26:33], v[224:231], v[58:61], v197, v198 op_sel_hi:[0,0,0]
	v_mfma_scale_f32_16x16x128_f8f6f4 v[50:53], v[18:25], v[224:231], v[50:53], v197, v198 op_sel_hi:[0,0,0]
	v_mfma_scale_f32_16x16x128_f8f6f4 v[42:45], v[26:33], v[232:239], v[42:45], v197, v198 op_sel_hi:[0,0,0]
	v_mfma_scale_f32_16x16x128_f8f6f4 v[34:37], v[18:25], v[232:239], v[34:37], v197, v198 op_sel_hi:[0,0,0]
	s_setprio 0
	s_setprio 1
	s_nop 3
	v_mfma_scale_f32_16x16x128_f8f6f4 v[102:105], v[10:17], v[208:215], v[102:105], v197, v198 op_sel_hi:[0,0,0]
	v_mfma_scale_f32_16x16x128_f8f6f4 v[90:93], v[2:9], v[208:215], v[90:93], v197, v198 op_sel_hi:[0,0,0]
	v_mfma_scale_f32_16x16x128_f8f6f4 v[86:89], v[10:17], v[216:223], v[86:89], v197, v198 op_sel_hi:[0,0,0]
	v_mfma_scale_f32_16x16x128_f8f6f4 v[74:77], v[2:9], v[216:223], v[74:77], v197, v198 op_sel_hi:[0,0,0]
	v_mfma_scale_f32_16x16x128_f8f6f4 v[62:65], v[10:17], v[224:231], v[62:65], v197, v198 op_sel_hi:[0,0,0]
	v_mfma_scale_f32_16x16x128_f8f6f4 v[54:57], v[2:9], v[224:231], v[54:57], v197, v198 op_sel_hi:[0,0,0]
	v_mfma_scale_f32_16x16x128_f8f6f4 v[46:49], v[10:17], v[232:239], v[46:49], v197, v198 op_sel_hi:[0,0,0]
	v_mfma_scale_f32_16x16x128_f8f6f4 v[38:41], v[2:9], v[232:239], v[38:41], v197, v198 op_sel_hi:[0,0,0]
	s_setprio 0
	s_barrier
; #define PG8_STAGE(bufoff, gbase, voff) do { _Pragma("unroll") for (int _i = 0; _i < 2; ++_i) \
;         __builtin_amdgcn_global_load_lds((const unsigned*)((const char*)(gbase) + (voff)[_i]), (PG8_LAS unsigned*)(lds + (bufoff) + ldsw + _i * 8192), 16, 0, 0); } while (0)
; #define PG8_STAGE_A(bufoff, gbase, h, nx) do { if constexpr (Sched::GATHER) { const unsigned vv_[2] = {(nx) ? vAn[h][0] : vA[h][0], (nx) ? vAn[h][1] : vA[h][1]}; PG8_STAGE(bufoff, gbase, vv_); } \
;         else { PG8_STAGE(bufoff, (gbase) + (h) * hstep, voffA); } } while (0)
; #define PG8_LDA(dst, b, h) do { _Pragma("unroll") for (int m = 0; m < 4; ++m) _Pragma("unroll") for (int k = 0; k < 2; ++k) dst[m][k] = *(const PG8_LAS bf16x8*)(lds + PG8_SA(b, h) + aoff + m * 2048 + k * 1024); } while (0)
; #define PG8_LDB(dst, b, h) do { _Pragma("unroll") for (int n = 0; n < 2; ++n) _Pragma("unroll") for (int k = 0; k < 2; ++k) dst[n][k] = *(const PG8_LAS bf16x8*)(lds + PG8_SB(b, h) + boff + n * 2048 + k * 1024); } while (0)
; #define PG8_WAIT_V(n) asm volatile("s_waitcnt vmcnt(" #n ")" ::: "memory")
; #define PG8_WAIT_L(n) asm volatile("s_waitcnt lgkmcnt(" #n ")" ::: "memory")
; #define PG8_BAR __builtin_amdgcn_s_barrier()
; #define PG8_SCHED __builtin_amdgcn_sched_barrier(0)
;     ...
;         for (int t = 0; t < nt; t += 2) {
;     ...
;             PG8_LDB(B0, 1, 0); PG8_LDB(B1, 1, 1); PG8_SCHED; PG8_LDA(At, 1, 0); PG8_STAGE_A(PG8_SA(0, 1), a2, 1, last);
;             PG8_WAIT_V(8); PG8_WAIT_L(0); PG8_BAR; PG8_MMA(0, 0, At, B0); PG8_MMA(0, 1, At, B1); PG8_BAR; PG8_SCHED;
;             PG8_LDA(At, 1, 1); PG8_STAGE(PG8_SB(1, 0), b3, voffB); PG8_STAGE(PG8_SB(1, 1), b3 + hstepB, voffB); PG8_STAGE_A(PG8_SA(1, 0), a3, 0, last);
;             PG8_WAIT_V(8); PG8_WAIT_L(0); PG8_BAR; PG8_MMA(1, 0, At, B0); PG8_MMA(1, 1, At, B1); PG8_BAR; PG8_SCHED;
	ds_read_b128 v[2:5], v199
	ds_read_b128 v[6:9], v199 offset:1024
	ds_read_b128 v[10:13], v199 offset:2048
	ds_read_b128 v[14:17], v199 offset:3072
	ds_read_b128 v[18:21], v200
	ds_read_b128 v[22:25], v200 offset:1024
	ds_read_b128 v[26:29], v200 offset:2048
	ds_read_b128 v[30:33], v200 offset:3072
	s_mov_b32 m0, s28
	v_cndmask_b32_e32 v166, v174, v204, vcc
	ds_read_b128 v[208:211], v196 offset:32768
	ds_read_b128 v[212:215], v196 offset:33792
	ds_read_b128 v[216:219], v196 offset:34816
	ds_read_b128 v[220:223], v196 offset:35840
	ds_read_b128 v[224:227], v196 offset:36864
	ds_read_b128 v[228:231], v196 offset:37888
	ds_read_b128 v[232:235], v196 offset:38912
	ds_read_b128 v[236:239], v196 offset:39936
	v_cndmask_b32_e32 v175, v176, v205, vcc
	global_load_lds_dwordx4 v166, s[22:23]
	s_mov_b32 m0, s29
	s_nop 0
	global_load_lds_dwordx4 v175, s[22:23]
	s_waitcnt vmcnt(8)
	s_waitcnt lgkmcnt(0)
	s_barrier
	s_setprio 1
	s_nop 3
	s_waitcnt lgkmcnt(0)
	v_mfma_scale_f32_16x16x128_f8f6f4 v[158:161], v[2:9], v[208:215], v[158:161], v197, v198 op_sel_hi:[0,0,0]
	v_mfma_scale_f32_16x16x128_f8f6f4 v[150:153], v[10:17], v[208:215], v[150:153], v197, v198 op_sel_hi:[0,0,0]
	v_mfma_scale_f32_16x16x128_f8f6f4 v[142:145], v[2:9], v[216:223], v[142:145], v197, v198 op_sel_hi:[0,0,0]
	v_mfma_scale_f32_16x16x128_f8f6f4 v[134:137], v[10:17], v[216:223], v[134:137], v197, v198 op_sel_hi:[0,0,0]
	v_mfma_scale_f32_16x16x128_f8f6f4 v[126:129], v[2:9], v[224:231], v[126:129], v197, v198 op_sel_hi:[0,0,0]
	v_mfma_scale_f32_16x16x128_f8f6f4 v[118:121], v[10:17], v[224:231], v[118:121], v197, v198 op_sel_hi:[0,0,0]
	v_mfma_scale_f32_16x16x128_f8f6f4 v[110:113], v[2:9], v[232:239], v[110:113], v197, v198 op_sel_hi:[0,0,0]
	v_mfma_scale_f32_16x16x128_f8f6f4 v[98:101], v[10:17], v[232:239], v[98:101], v197, v198 op_sel_hi:[0,0,0]
	s_setprio 0
	s_setprio 1
	s_nop 3
	v_mfma_scale_f32_16x16x128_f8f6f4 v[154:157], v[18:25], v[208:215], v[154:157], v197, v198 op_sel_hi:[0,0,0]
	v_mfma_scale_f32_16x16x128_f8f6f4 v[146:149], v[26:33], v[208:215], v[146:149], v197, v198 op_sel_hi:[0,0,0]
	v_mfma_scale_f32_16x16x128_f8f6f4 v[138:141], v[18:25], v[216:223], v[138:141], v197, v198 op_sel_hi:[0,0,0]
	v_mfma_scale_f32_16x16x128_f8f6f4 v[130:133], v[26:33], v[216:223], v[130:133], v197, v198 op_sel_hi:[0,0,0]
	v_mfma_scale_f32_16x16x128_f8f6f4 v[122:125], v[18:25], v[224:231], v[122:125], v197, v198 op_sel_hi:[0,0,0]
	v_mfma_scale_f32_16x16x128_f8f6f4 v[114:117], v[26:33], v[224:231], v[114:117], v197, v198 op_sel_hi:[0,0,0]
	v_mfma_scale_f32_16x16x128_f8f6f4 v[106:109], v[18:25], v[232:239], v[106:109], v197, v198 op_sel_hi:[0,0,0]
	v_mfma_scale_f32_16x16x128_f8f6f4 v[94:97], v[26:33], v[232:239], v[94:97], v197, v198 op_sel_hi:[0,0,0]
	s_setprio 0
	s_barrier
	s_mov_b32 m0, s45
	v_lshl_add_u64 v[182:183], v[182:183], 0, s[10:11]
	s_add_u32 s20, s20, 0x20080
	ds_read_b128 v[208:211], v196 offset:49152
	ds_read_b128 v[212:215], v196 offset:50176
	ds_read_b128 v[216:219], v196 offset:51200
	ds_read_b128 v[220:223], v196 offset:52224
	ds_read_b128 v[224:227], v196 offset:53248
	ds_read_b128 v[228:231], v196 offset:54272
	ds_read_b128 v[232:235], v196 offset:55296
	ds_read_b128 v[236:239], v196 offset:56320
	global_load_lds_dwordx4 v[182:183], off
	v_lshl_add_u64 v[182:183], v[184:185], 0, s[10:11]
	s_mov_b32 m0, s46
	s_addc_u32 s21, s21, 0
	global_load_lds_dwordx4 v[182:183], off
	v_lshl_add_u64 v[182:183], s[20:21], 0, v[164:165]
	s_mov_b32 m0, s47
	s_nop 0
	global_load_lds_dwordx4 v[182:183], off
	v_lshl_add_u64 v[182:183], s[20:21], 0, v[162:163]
	s_add_i32 m0, s47, 0x2000
	s_nop 0
	global_load_lds_dwordx4 v[182:183], off
	v_lshl_add_u64 v[182:183], v[188:189], 0, s[10:11]
	s_mov_b32 m0, s31
	s_nop 0
	global_load_lds_dwordx4 v[182:183], off
	v_lshl_add_u64 v[182:183], v[186:187], 0, s[10:11]
	s_mov_b32 m0, s34
	s_nop 0
	global_load_lds_dwordx4 v[182:183], off
	s_waitcnt vmcnt(8)
	s_waitcnt lgkmcnt(0)
	s_barrier
	s_setprio 1
	s_nop 3
	s_waitcnt lgkmcnt(0)
	v_mfma_scale_f32_16x16x128_f8f6f4 v[82:85], v[2:9], v[208:215], v[82:85], v197, v198 op_sel_hi:[0,0,0]
	v_mfma_scale_f32_16x16x128_f8f6f4 v[70:73], v[10:17], v[208:215], v[70:73], v197, v198 op_sel_hi:[0,0,0]
	v_mfma_scale_f32_16x16x128_f8f6f4 v[78:81], v[2:9], v[216:223], v[78:81], v197, v198 op_sel_hi:[0,0,0]
	v_mfma_scale_f32_16x16x128_f8f6f4 v[66:69], v[10:17], v[216:223], v[66:69], v197, v198 op_sel_hi:[0,0,0]
	v_mfma_scale_f32_16x16x128_f8f6f4 v[58:61], v[2:9], v[224:231], v[58:61], v197, v198 op_sel_hi:[0,0,0]
	v_mfma_scale_f32_16x16x128_f8f6f4 v[50:53], v[10:17], v[224:231], v[50:53], v197, v198 op_sel_hi:[0,0,0]
	v_mfma_scale_f32_16x16x128_f8f6f4 v[42:45], v[2:9], v[232:239], v[42:45], v197, v198 op_sel_hi:[0,0,0]
	v_mfma_scale_f32_16x16x128_f8f6f4 v[34:37], v[10:17], v[232:239], v[34:37], v197, v198 op_sel_hi:[0,0,0]
	s_setprio 0
	s_setprio 1
	s_nop 3
	v_mfma_scale_f32_16x16x128_f8f6f4 v[102:105], v[18:25], v[208:215], v[102:105], v197, v198 op_sel_hi:[0,0,0]
	v_mfma_scale_f32_16x16x128_f8f6f4 v[90:93], v[26:33], v[208:215], v[90:93], v197, v198 op_sel_hi:[0,0,0]
	v_mfma_scale_f32_16x16x128_f8f6f4 v[86:89], v[18:25], v[216:223], v[86:89], v197, v198 op_sel_hi:[0,0,0]
	v_mfma_scale_f32_16x16x128_f8f6f4 v[74:77], v[26:33], v[216:223], v[74:77], v197, v198 op_sel_hi:[0,0,0]
	v_mfma_scale_f32_16x16x128_f8f6f4 v[62:65], v[18:25], v[224:231], v[62:65], v197, v198 op_sel_hi:[0,0,0]
	v_mfma_scale_f32_16x16x128_f8f6f4 v[54:57], v[26:33], v[224:231], v[54:57], v197, v198 op_sel_hi:[0,0,0]
	v_mfma_scale_f32_16x16x128_f8f6f4 v[46:49], v[18:25], v[232:239], v[46:49], v197, v198 op_sel_hi:[0,0,0]
	v_mfma_scale_f32_16x16x128_f8f6f4 v[38:41], v[26:33], v[232:239], v[38:41], v197, v198 op_sel_hi:[0,0,0]
	s_setprio 0
	s_add_i32 s54, s54, 2
	s_add_u32 s4, s4, 0x100
	s_addc_u32 s5, s5, 0
	s_cmp_gt_u32 s54, 5
	s_barrier
	s_cbranch_scc0 .LBB0_1572
	s_and_b64 vcc, exec, s[14:15]
	s_cbranch_vccz .LBB0_1575
	s_barrier

; #define PG8_STAGE(bufoff, gbase, voff) do { _Pragma("unroll") for (int _i = 0; _i < 2; ++_i) \
;         __builtin_amdgcn_global_load_lds((const unsigned*)((const char*)(gbase) + (voff)[_i]), (PG8_LAS unsigned*)(lds + (bufoff) + ldsw + _i * 8192), 16, 0, 0); } while (0)
; #define PG8_STAGE_A(bufoff, gbase, h, nx) do { if constexpr (Sched::GATHER) { const unsigned vv_[2] = {(nx) ? vAn[h][0] : vA[h][0], (nx) ? vAn[h][1] : vA[h][1]}; PG8_STAGE(bufoff, gbase, vv_); } \
;         else { PG8_STAGE(bufoff, (gbase) + (h) * hstep, voffA); } } while (0)
; #define PG8_LDA(dst, b, h) do { _Pragma("unroll") for (int m = 0; m < 4; ++m) _Pragma("unroll") for (int k = 0; k < 2; ++k) dst[m][k] = *(const PG8_LAS bf16x8*)(lds + PG8_SA(b, h) + aoff + m * 2048 + k * 1024); } while (0)
; #define PG8_WAIT_V(n) asm volatile("s_waitcnt vmcnt(" #n ")" ::: "memory")
; #define PG8_WAIT_L(n) asm volatile("s_waitcnt lgkmcnt(" #n ")" ::: "memory")
; #define PG8_BAR __builtin_amdgcn_s_barrier()
; #define PG8_SCHED __builtin_amdgcn_sched_barrier(0)
;     ...
;         for (int t = 0; t < nt; t += 2) {
;     ...
;             PG8_WAIT_V(8); PG8_WAIT_L(0); PG8_BAR; PG8_MMA(0, 0, At, B0); PG8_MMA(0, 1, At, B1); PG8_BAR; PG8_SCHED;
;             PG8_LDA(At, 1, 1); PG8_STAGE(PG8_SB(1, 0), b3, voffB); PG8_STAGE(PG8_SB(1, 1), b3 + hstepB, voffB); PG8_STAGE_A(PG8_SA(1, 0), a3, 0, last);
;             PG8_WAIT_V(8); PG8_WAIT_L(0); PG8_BAR; PG8_MMA(1, 0, At, B0); PG8_MMA(1, 1, At, B1); PG8_BAR; PG8_SCHED;
.Lgate19_skip:
	s_waitcnt lgkmcnt(0)
	s_barrier
	s_setprio 1
	s_nop 3
	s_waitcnt lgkmcnt(0)
	v_mfma_scale_f32_16x16x128_f8f6f4 v[94:97], v[2:9], v[194:201], v[94:97], v191, v192 op_sel_hi:[0,0,0]
	v_mfma_scale_f32_16x16x128_f8f6f4 v[90:93], v[10:17], v[194:201], v[90:93], v191, v192 op_sel_hi:[0,0,0]
	v_mfma_scale_f32_16x16x128_f8f6f4 v[78:81], v[2:9], v[202:209], v[78:81], v191, v192 op_sel_hi:[0,0,0]
	v_mfma_scale_f32_16x16x128_f8f6f4 v[74:77], v[10:17], v[202:209], v[74:77], v191, v192 op_sel_hi:[0,0,0]
	v_mfma_scale_f32_16x16x128_f8f6f4 v[62:65], v[2:9], v[210:217], v[62:65], v191, v192 op_sel_hi:[0,0,0]
	v_mfma_scale_f32_16x16x128_f8f6f4 v[58:61], v[10:17], v[210:217], v[58:61], v191, v192 op_sel_hi:[0,0,0]
	v_mfma_scale_f32_16x16x128_f8f6f4 v[46:49], v[2:9], v[218:225], v[46:49], v191, v192 op_sel_hi:[0,0,0]
	v_mfma_scale_f32_16x16x128_f8f6f4 v[42:45], v[10:17], v[218:225], v[42:45], v191, v192 op_sel_hi:[0,0,0]
	s_setprio 0
	s_setprio 1
	s_nop 3
	v_mfma_scale_f32_16x16x128_f8f6f4 v[86:89], v[18:25], v[194:201], v[86:89], v191, v192 op_sel_hi:[0,0,0]
	v_mfma_scale_f32_16x16x128_f8f6f4 v[82:85], v[26:33], v[194:201], v[82:85], v191, v192 op_sel_hi:[0,0,0]
	v_mfma_scale_f32_16x16x128_f8f6f4 v[70:73], v[18:25], v[202:209], v[70:73], v191, v192 op_sel_hi:[0,0,0]
	v_mfma_scale_f32_16x16x128_f8f6f4 v[66:69], v[26:33], v[202:209], v[66:69], v191, v192 op_sel_hi:[0,0,0]
	v_mfma_scale_f32_16x16x128_f8f6f4 v[54:57], v[18:25], v[210:217], v[54:57], v191, v192 op_sel_hi:[0,0,0]
	v_mfma_scale_f32_16x16x128_f8f6f4 v[50:53], v[26:33], v[210:217], v[50:53], v191, v192 op_sel_hi:[0,0,0]
	v_mfma_scale_f32_16x16x128_f8f6f4 v[38:41], v[18:25], v[218:225], v[38:41], v191, v192 op_sel_hi:[0,0,0]
	v_mfma_scale_f32_16x16x128_f8f6f4 v[34:37], v[26:33], v[218:225], v[34:37], v191, v192 op_sel_hi:[0,0,0]
	s_setprio 0
	s_add_i32 s50, s50, 2
	s_add_u32 s22, s22, 0x100
	s_addc_u32 s23, s23, 0
	s_add_u32 s48, s48, 0x100
	s_addc_u32 s49, s49, 0
	s_cmp_gt_u32 s50, 13
	s_barrier
	s_cbranch_scc0 .LBB0_1626
	s_and_b64 vcc, exec, s[10:11]
	s_cbranch_vccz .LBB0_1629
	s_barrier
